# E5: E4 + NSA tile loops: fmax canonicalisation copies removed (exact for non-sNaN) and LDS waits re-derived as counted lgkmcnt; loop headers nop-aligned to baseline
# speedup vs baseline: 1.0076x; 1.0072x over previous
.LBB0_524:
	s_add_i32 s2, s22, 0
	v_add_u32_e32 v0, s2, v140
	ds_read_b128 v[4:7], v0
	ds_read_b128 v[8:11], v0 offset:4096
	ds_read_b128 v[12:15], v197
	ds_read_b128 v[16:19], v197 offset:4096
	ds_read_b128 v[20:23], v0 offset:8192
	ds_read_b128 v[28:31], v0 offset:12288
	s_waitcnt lgkmcnt(0)
	v_mfma_f32_16x16x32_bf16 v[24:27], v[4:7], v[12:15], 0
	v_mfma_f32_16x16x32_bf16 v[4:7], v[4:7], v[16:19], 0
	v_add_u32_e32 v0, s2, v143
	ds_read_b128 v[48:51], v0
	ds_read_b128 v[52:55], v197 offset:1024
	ds_read_b128 v[56:59], v197 offset:5120
	v_mfma_f32_16x16x32_bf16 v[32:35], v[8:11], v[12:15], 0
	v_mfma_f32_16x16x32_bf16 v[8:11], v[8:11], v[16:19], 0
	v_mfma_f32_16x16x32_bf16 v[60:63], v[20:23], v[12:15], 0
	ds_read_b128 v[64:67], v0 offset:4096
	v_mfma_f32_16x16x32_bf16 v[20:23], v[20:23], v[16:19], 0
	v_mfma_f32_16x16x32_bf16 v[12:15], v[28:31], v[12:15], 0
	v_mfma_f32_16x16x32_bf16 v[16:19], v[28:31], v[16:19], 0
	ds_read_b128 v[28:31], v0 offset:8192
	s_waitcnt lgkmcnt(3)
	v_mfma_f32_16x16x32_bf16 v[24:27], v[48:51], v[52:55], v[24:27]
	s_waitcnt lgkmcnt(2)
	v_mfma_f32_16x16x32_bf16 v[4:7], v[48:51], v[56:59], v[4:7]
	ds_read_b128 v[48:51], v0 offset:12288
	v_add_u32_e32 v0, s2, v144
	s_waitcnt lgkmcnt(2)
	v_mfma_f32_16x16x32_bf16 v[32:35], v[64:67], v[52:55], v[32:35]
	v_mfma_f32_16x16x32_bf16 v[8:11], v[64:67], v[56:59], v[8:11]
	ds_read_b128 v[64:67], v0
	ds_read_b128 v[68:71], v197 offset:2048
	ds_read_b128 v[72:75], v197 offset:6144
	s_waitcnt lgkmcnt(4)
	v_mfma_f32_16x16x32_bf16 v[60:63], v[28:31], v[52:55], v[60:63]
	v_mfma_f32_16x16x32_bf16 v[20:23], v[28:31], v[56:59], v[20:23]
	ds_read_b128 v[28:31], v0 offset:4096
	s_waitcnt lgkmcnt(4)
	v_mfma_f32_16x16x32_bf16 v[12:15], v[48:51], v[52:55], v[12:15]
	ds_read_b128 v[52:55], v0 offset:8192
	v_mfma_f32_16x16x32_bf16 v[16:19], v[48:51], v[56:59], v[16:19]
	ds_read_b128 v[48:51], v0 offset:12288
	s_waitcnt lgkmcnt(4)
	v_mfma_f32_16x16x32_bf16 v[24:27], v[64:67], v[68:71], v[24:27]
	s_waitcnt lgkmcnt(3)
	v_mfma_f32_16x16x32_bf16 v[4:7], v[64:67], v[72:75], v[4:7]
	v_add_u32_e32 v0, s2, v145
	s_waitcnt lgkmcnt(2)
	v_mfma_f32_16x16x32_bf16 v[56:59], v[28:31], v[68:71], v[32:35]
	v_mfma_f32_16x16x32_bf16 v[8:11], v[28:31], v[72:75], v[8:11]
	ds_read_b128 v[28:31], v0
	ds_read_b128 v[64:67], v197 offset:3072
	ds_read_b128 v[76:79], v197 offset:7168
	s_waitcnt lgkmcnt(4)
	v_mfma_f32_16x16x32_bf16 v[60:63], v[52:55], v[68:71], v[60:63]
	v_mfma_f32_16x16x32_bf16 v[20:23], v[52:55], v[72:75], v[20:23]
	ds_read_b128 v[52:55], v0 offset:4096
	s_waitcnt lgkmcnt(4)
	v_mfma_f32_16x16x32_bf16 v[68:71], v[48:51], v[68:71], v[12:15]
	ds_read_b128 v[80:83], v0 offset:8192
	v_mfma_f32_16x16x32_bf16 v[48:51], v[48:51], v[72:75], v[16:19]
	s_waitcnt lgkmcnt(2)
	v_mfma_f32_16x16x32_bf16 v[16:19], v[28:31], v[76:79], v[4:7]
	s_nop 2
	ds_read_b128 v[4:7], v0 offset:12288
	v_mfma_f32_16x16x32_bf16 v[32:35], v[28:31], v[64:67], v[24:27]
	s_waitcnt lgkmcnt(2)
	v_mfma_f32_16x16x32_bf16 v[28:31], v[52:55], v[64:67], v[56:59]
	v_mfma_f32_16x16x32_bf16 v[12:15], v[52:55], v[76:79], v[8:11]
	s_waitcnt lgkmcnt(1)
	v_mfma_f32_16x16x32_bf16 v[24:27], v[80:83], v[64:67], v[60:63]
	v_mfma_f32_16x16x32_bf16 v[8:11], v[80:83], v[76:79], v[20:23]
	s_waitcnt lgkmcnt(0)
	v_mfma_f32_16x16x32_bf16 v[20:23], v[4:7], v[64:67], v[68:71]
	v_mfma_f32_16x16x32_bf16 v[4:7], v[4:7], v[76:79], v[48:51]
	s_nop 2
	v_add_u32_e32 v50, s0, v195
	v_subrev_u32_e32 v51, 31, v50
	v_cmp_lt_i32_e32 vcc, -1, v51
	v_mov_b32_e32 v48, 0xff800000
	v_mov_b32_e32 v49, 0xff800000
	s_and_saveexec_b64 s[2:3], vcc
	s_cbranch_execz .LBB0_526
	v_min_u32_e32 v0, 0x7f, v51
	v_lshl_add_u32 v0, v0, 2, v196
	ds_read_b32 v49, v0
	s_waitcnt lgkmcnt(0)
	v_fmac_f32_e32 v49, 0x3fb8aa3b, v32

.LBB0_588:
	s_or_b64 exec, exec, s[2:3]
	v_max_f32_e32 v0, v49, v48
	v_max3_f32 v0, v0, v33, v32
	v_max3_f32 v0, v0, v35, v34
	v_max3_f32 v0, v0, v29, v28
	v_max3_f32 v0, v0, v31, v30
	v_max3_f32 v0, v0, v25, v24
	v_max3_f32 v0, v0, v27, v26
	v_max3_f32 v0, v0, v21, v20
	v_mov_b32_e32 v6, v0
	s_nop 1
	v_permlane16_swap_b32_e32 v0, v6
	v_max_f32_e32 v0, v0, v6
	v_mov_b32_e32 v6, v0
	s_nop 1
	v_permlane32_swap_b32_e32 v0, v6
	v_max3_f32 v198, v47, v0, v6
	v_sub_f32_e32 v0, v49, v198
	v_exp_f32_e32 v0, v0
	v_sub_f32_e32 v6, v48, v198
	v_exp_f32_e32 v6, v6
	v_sub_f32_e32 v7, v32, v198
	v_add_f32_e32 v0, 0, v0
	v_exp_f32_e32 v7, v7
	v_add_f32_e32 v0, v6, v0
	v_sub_f32_e32 v6, v33, v198
	v_exp_f32_e32 v6, v6
	v_sub_f32_e32 v32, v35, v198
	v_exp_f32_e32 v32, v32
	v_sub_f32_e32 v33, v34, v198
	v_exp_f32_e32 v33, v33
	v_add_f32_e32 v0, v6, v0
	v_add_f32_e32 v0, v7, v0
	v_add_f32_e32 v0, v32, v0
	v_add_f32_e32 v7, v33, v0
	v_sub_f32_e32 v0, v29, v198
	v_exp_f32_e32 v29, v0
	v_sub_f32_e32 v0, v28, v198
	v_exp_f32_e32 v33, v0
	v_sub_f32_e32 v0, v31, v198
	v_exp_f32_e32 v31, v0
	v_sub_f32_e32 v0, v30, v198
	v_exp_f32_e32 v35, v0
	v_sub_f32_e32 v0, v25, v198
	v_exp_f32_e32 v25, v0
	v_sub_f32_e32 v0, v24, v198
	v_sub_f32_e32 v48, v47, v198
	v_exp_f32_e32 v47, v0
	v_sub_f32_e32 v0, v27, v198
	v_exp_f32_e32 v27, v0
	v_sub_f32_e32 v0, v26, v198
	v_exp_f32_e32 v49, v0
	v_sub_f32_e32 v0, v21, v198
	v_exp_f32_e32 v21, v0
	v_sub_f32_e32 v0, v20, v198
	v_exp_f32_e32 v51, v0
	v_max_f32_e32 v0, v23, v22
	v_max3_f32 v0, v0, v17, v16
	v_max3_f32 v0, v0, v19, v18
	v_max3_f32 v0, v0, v13, v12
	v_max3_f32 v0, v0, v15, v14
	v_max3_f32 v0, v0, v9, v8
	v_max3_f32 v0, v0, v11, v10
	v_max3_f32 v0, v0, v5, v4
	v_mov_b32_e32 v6, v0
	s_nop 1
	v_permlane16_swap_b32_e32 v0, v6
	v_max_f32_e32 v0, v0, v6
	v_mov_b32_e32 v6, v0
	s_nop 1
	v_permlane32_swap_b32_e32 v0, v6
	v_max3_f32 v199, v46, v0, v6
	v_sub_f32_e32 v0, v23, v199
	v_exp_f32_e32 v0, v0
	v_sub_f32_e32 v6, v22, v199
	v_exp_f32_e32 v6, v6
	v_sub_f32_e32 v16, v16, v199
	v_add_f32_e32 v0, 0, v0
	v_exp_f32_e32 v16, v16
	v_add_f32_e32 v0, v6, v0
	v_sub_f32_e32 v6, v17, v199
	v_exp_f32_e32 v6, v6
	v_sub_f32_e32 v17, v19, v199
	v_exp_f32_e32 v17, v17
	v_sub_f32_e32 v18, v18, v199
	v_exp_f32_e32 v18, v18
	v_add_f32_e32 v0, v6, v0
	v_add_f32_e32 v0, v16, v0
	v_add_f32_e32 v0, v17, v0
	v_add_f32_e32 v6, v18, v0
	v_sub_f32_e32 v0, v13, v199
	v_exp_f32_e32 v28, v0
	v_sub_f32_e32 v0, v12, v199
	v_exp_f32_e32 v32, v0
	v_sub_f32_e32 v0, v15, v199
	v_exp_f32_e32 v30, v0
	v_sub_f32_e32 v0, v14, v199
	v_exp_f32_e32 v34, v0
	v_sub_f32_e32 v0, v9, v199
	v_exp_f32_e32 v24, v0
	v_sub_f32_e32 v0, v8, v199
	v_sub_f32_e32 v22, v46, v199
	v_exp_f32_e32 v46, v0
	v_sub_f32_e32 v0, v11, v199
	v_exp_f32_e32 v26, v0
	v_sub_f32_e32 v0, v10, v199
	v_exp_f32_e32 v23, v48
	v_exp_f32_e32 v48, v0
	v_sub_f32_e32 v0, v5, v199
	v_exp_f32_e32 v20, v0
	v_sub_f32_e32 v0, v4, v199
	v_pk_add_f32 v[4:5], v[28:29], v[6:7]
	v_exp_f32_e32 v50, v0
	v_pk_add_f32 v[4:5], v[32:33], v[4:5]
	v_exp_f32_e32 v22, v22
	v_pk_add_f32 v[4:5], v[30:31], v[4:5]
	s_waitcnt vmcnt(0)
	s_addk_i32 s0, 0xfc00
	v_pk_add_f32 v[4:5], v[34:35], v[4:5]
	s_add_i32 s2, s96, s0
	v_pk_add_f32 v[4:5], v[24:25], v[4:5]
	s_add_i32 s1, s1, 1
	v_pk_add_f32 v[4:5], v[46:47], v[4:5]
	v_lshl_add_u64 v[42:43], v[42:43], 0, s[12:13]
	v_pk_add_f32 v[4:5], v[26:27], v[4:5]
	s_cmp_lg_u32 s2, 0
	v_pk_add_f32 v[4:5], v[48:49], v[4:5]
	v_lshl_add_u64 v[44:45], v[44:45], 0, s[12:13]
	v_pk_add_f32 v[4:5], v[20:21], v[4:5]
	s_waitcnt vmcnt(0)
	v_pk_add_f32 v[4:5], v[50:51], v[4:5]
	s_barrier
	v_pk_fma_f32 v[40:41], v[40:41], v[22:23], v[4:5]
	s_cbranch_scc1 .LBB0_520
	v_mov_b32_e32 v0, v41
	s_nop 1
	v_permlane16_swap_b32_e32 v41, v0
	v_add_f32_e32 v5, v41, v0
	v_mov_b32_e32 v0, v40
	s_nop 1
	v_permlane16_swap_b32_e32 v40, v0
	v_add_f32_e32 v4, v40, v0
	v_mov_b32_e32 v7, v5
	v_mov_b32_e32 v6, v4
	s_nop 0
	v_permlane32_swap_b32_e32 v5, v7
	v_permlane32_swap_b32_e32 v4, v6
	v_pk_add_f32 v[6:7], v[4:5], v[6:7]
	s_mov_b32 m0, s28
	v_div_scale_f32 v0, s[0:1], v7, v7, 1.0
	v_rcp_f32_e32 v4, v0
	v_readlane_b32 s0, v253, 8
	s_add_u32 s0, s0, s37
	v_readlane_b32 s1, v253, 10
	v_fma_f32 v5, -v0, v4, 1.0
	v_fmac_f32_e32 v4, v5, v4
	v_div_scale_f32 v5, vcc, 1.0, v7, 1.0
	v_mul_f32_e32 v8, v5, v4
	v_fma_f32 v9, -v0, v8, v5
	v_fmac_f32_e32 v8, v9, v4
	v_fma_f32 v0, -v0, v8, v5
	v_div_scale_f32 v5, s[2:3], v6, v6, 1.0
	v_div_fmas_f32 v0, v0, v4, v8
	v_rcp_f32_e32 v8, v5
	v_div_fixup_f32 v0, v0, v7, 1.0
	v_cmp_lt_f32_e32 vcc, 0, v7
	s_addc_u32 s1, s1, 0
	global_load_lds_dwordx4 v[36:37], off
	v_cndmask_b32_e32 v100, 0, v0, vcc
	v_fma_f32 v0, -v5, v8, 1.0
	v_fmac_f32_e32 v8, v0, v8
	v_div_scale_f32 v0, vcc, 1.0, v6, 1.0
	v_mul_f32_e32 v7, v0, v8
	v_fma_f32 v9, -v5, v7, v0
	v_fmac_f32_e32 v7, v9, v8
	v_fma_f32 v0, -v5, v7, v0
	s_mov_b32 m0, s81
	v_div_fmas_f32 v0, v0, v8, v7
	global_load_lds_dwordx4 v[38:39], off
	v_lshl_add_u64 v[8:9], s[0:1], 0, v[104:105]
	s_mov_b32 m0, s77
	v_div_fixup_f32 v0, v0, v6, 1.0
	global_load_lds_dwordx4 v[8:9], off
	v_lshl_add_u64 v[8:9], s[0:1], 0, v[110:111]
	s_mov_b32 m0, s78
	v_cmp_lt_f32_e32 vcc, 0, v6
	global_load_lds_dwordx4 v[8:9], off
	s_waitcnt vmcnt(0)
	v_mov_b32_e32 v4, 0
	v_cndmask_b32_e32 v128, 0, v0, vcc
	v_mov_b32_e32 v129, v128
	v_mov_b32_e32 v101, v100
	s_mov_b32 s2, 0
	v_mov_b32_e32 v200, v154
	v_mov_b32_e32 v201, v153
	v_mov_b64_e32 v[130:131], v[116:117]
	v_mov_b64_e32 v[132:133], v[118:119]
	v_mov_b64_e32 v[134:135], v[122:123]
	v_mov_b64_e32 v[136:137], v[120:121]
	s_mov_b32 s3, 0
	v_mov_b32_e32 v5, v4
	v_mov_b32_e32 v6, v4
	v_mov_b32_e32 v7, v4
	v_mov_b32_e32 v8, v4
	v_mov_b32_e32 v9, v4
	v_mov_b32_e32 v10, v4
	v_mov_b32_e32 v11, v4
	v_mov_b32_e32 v12, v4
	v_mov_b32_e32 v13, v4
	v_mov_b32_e32 v14, v4
	v_mov_b32_e32 v15, v4
	v_mov_b32_e32 v16, v4
	v_mov_b32_e32 v17, v4
	v_mov_b32_e32 v18, v4
	v_mov_b32_e32 v19, v4
	v_mov_b32_e32 v20, v4
	v_mov_b32_e32 v21, v4
	v_mov_b32_e32 v22, v4
	v_mov_b32_e32 v23, v4
	v_mov_b32_e32 v24, v4
	v_mov_b32_e32 v25, v4
	v_mov_b32_e32 v26, v4
	v_mov_b32_e32 v27, v4
	v_mov_b32_e32 v28, v4
	v_mov_b32_e32 v29, v4
	v_mov_b32_e32 v30, v4
	v_mov_b32_e32 v31, v4
	v_mov_b32_e32 v32, v4
	v_mov_b32_e32 v33, v4
	v_mov_b32_e32 v34, v4
	v_mov_b32_e32 v35, v4
	v_mov_b32_e32 v36, v4
	v_mov_b32_e32 v37, v4
	v_mov_b32_e32 v38, v4
	v_mov_b32_e32 v39, v4
	v_mov_b32_e32 v40, v4
	v_mov_b32_e32 v41, v4
	v_mov_b32_e32 v42, v4
	v_mov_b32_e32 v43, v4
	v_mov_b32_e32 v44, v4
	v_mov_b32_e32 v45, v4
	v_mov_b32_e32 v46, v4
	v_mov_b32_e32 v47, v4
	v_mov_b32_e32 v48, v4
	v_mov_b32_e32 v49, v4
	v_mov_b32_e32 v50, v4
	v_mov_b32_e32 v51, v4
	v_mov_b32_e32 v52, v4
	v_mov_b32_e32 v53, v4
	v_mov_b32_e32 v54, v4
	v_mov_b32_e32 v55, v4
	v_mov_b32_e32 v56, v4
	v_mov_b32_e32 v57, v4
	v_mov_b32_e32 v58, v4
	v_mov_b32_e32 v59, v4
	v_mov_b32_e32 v60, v4
	v_mov_b32_e32 v61, v4
	v_mov_b32_e32 v62, v4
	v_mov_b32_e32 v63, v4
	v_mov_b32_e32 v64, v4
	v_mov_b32_e32 v65, v4
	v_mov_b32_e32 v66, v4
	v_mov_b32_e32 v67, v4
	s_waitcnt vmcnt(0) lgkmcnt(0)
	s_barrier
	s_branch .LBB0_591
	s_nop 0
	s_nop 0
	s_nop 0
	s_nop 0
	s_nop 0
	s_nop 0
	s_nop 0
	s_nop 0
	s_nop 0
	s_nop 0
	s_nop 0
	s_nop 0
	s_nop 0
	s_nop 0
.LBB0_590:
	s_or_b64 exec, exec, s[0:1]
	s_cmp_eq_u32 s33, 0
	s_cselect_b32 s0, 0x8000, s79
	s_add_i32 s0, s0, 0
	v_add_u32_e32 v0, s0, v142
	ds_read_b128 v[202:205], v0
	ds_read_b128 v[206:209], v0 offset:2048
	v_cvt_pk_bf16_f32 v72, v72, v73
	v_cvt_pk_bf16_f32 v73, v74, v75
	v_cvt_pk_bf16_f32 v74, v80, v81
	v_cvt_pk_bf16_f32 v75, v82, v83
	ds_read_b128 v[80:83], v0 offset:4096
	v_cvt_pk_bf16_f32 v88, v88, v89
	v_cvt_pk_bf16_f32 v89, v90, v91
	v_cvt_pk_bf16_f32 v90, v96, v97
	v_cvt_pk_bf16_f32 v91, v98, v99
	s_waitcnt lgkmcnt(0)
	v_mfma_f32_16x16x32_bf16 v[64:67], v[202:205], v[72:75], v[64:67]
	ds_read_b128 v[96:99], v0 offset:6144
	v_mfma_f32_16x16x32_bf16 v[32:35], v[202:205], v[88:91], v[32:35]
	v_mfma_f32_16x16x32_bf16 v[60:63], v[206:209], v[72:75], v[60:63]
	ds_read_b128 v[202:205], v0 offset:8192
	v_mfma_f32_16x16x32_bf16 v[28:31], v[206:209], v[88:91], v[28:31]
	v_mfma_f32_16x16x32_bf16 v[56:59], v[80:83], v[72:75], v[56:59]
	v_mfma_f32_16x16x32_bf16 v[24:27], v[80:83], v[88:91], v[24:27]
	ds_read_b128 v[80:83], v0 offset:10240
	s_waitcnt lgkmcnt(2)
	v_mfma_f32_16x16x32_bf16 v[52:55], v[96:99], v[72:75], v[52:55]
	v_mfma_f32_16x16x32_bf16 v[20:23], v[96:99], v[88:91], v[20:23]
	ds_read_b128 v[96:99], v0 offset:12288
	s_waitcnt lgkmcnt(2)
	v_mfma_f32_16x16x32_bf16 v[48:51], v[202:205], v[72:75], v[48:51]
	v_mfma_f32_16x16x32_bf16 v[16:19], v[202:205], v[88:91], v[16:19]
	ds_read_b128 v[202:205], v0 offset:14336
	v_add_u32_e32 v0, s0, v146
	s_waitcnt lgkmcnt(2)
	v_mfma_f32_16x16x32_bf16 v[44:47], v[80:83], v[72:75], v[44:47]
	v_mfma_f32_16x16x32_bf16 v[12:15], v[80:83], v[88:91], v[12:15]
	ds_read_b128 v[80:83], v0
	s_waitcnt lgkmcnt(2)
	v_mfma_f32_16x16x32_bf16 v[40:43], v[96:99], v[72:75], v[40:43]
	v_mfma_f32_16x16x32_bf16 v[8:11], v[96:99], v[88:91], v[8:11]
	ds_read_b128 v[96:99], v0 offset:2048
	s_waitcnt lgkmcnt(2)
	v_mfma_f32_16x16x32_bf16 v[36:39], v[202:205], v[72:75], v[36:39]
	ds_read_b128 v[72:75], v0 offset:4096
	v_cvt_pk_bf16_f32 v68, v68, v69
	v_cvt_pk_bf16_f32 v69, v70, v71
	v_mfma_f32_16x16x32_bf16 v[4:7], v[202:205], v[88:91], v[4:7]
	v_cvt_pk_bf16_f32 v70, v76, v77
	v_cvt_pk_bf16_f32 v71, v78, v79
	v_cvt_pk_bf16_f32 v76, v84, v85
	v_cvt_pk_bf16_f32 v77, v86, v87
	v_cvt_pk_bf16_f32 v78, v92, v93
	v_cvt_pk_bf16_f32 v79, v94, v95
	s_waitcnt lgkmcnt(2)
	v_mfma_f32_16x16x32_bf16 v[64:67], v[80:83], v[68:71], v[64:67]
	s_nop 0
	v_mfma_f32_16x16x32_bf16 v[32:35], v[80:83], v[76:79], v[32:35]
	ds_read_b128 v[80:83], v0 offset:6144
	s_waitcnt lgkmcnt(2)
	v_mfma_f32_16x16x32_bf16 v[60:63], v[96:99], v[68:71], v[60:63]
	ds_read_b128 v[84:87], v0 offset:8192
	v_mfma_f32_16x16x32_bf16 v[28:31], v[96:99], v[76:79], v[28:31]
	s_waitcnt lgkmcnt(2)
	v_mfma_f32_16x16x32_bf16 v[56:59], v[72:75], v[68:71], v[56:59]
	v_mfma_f32_16x16x32_bf16 v[24:27], v[72:75], v[76:79], v[24:27]
	ds_read_b128 v[72:75], v0 offset:10240
	s_waitcnt lgkmcnt(2)
	v_mfma_f32_16x16x32_bf16 v[52:55], v[80:83], v[68:71], v[52:55]
	v_mfma_f32_16x16x32_bf16 v[20:23], v[80:83], v[76:79], v[20:23]
	ds_read_b128 v[80:83], v0 offset:12288
	s_waitcnt lgkmcnt(2)
	v_mfma_f32_16x16x32_bf16 v[48:51], v[84:87], v[68:71], v[48:51]
	v_mfma_f32_16x16x32_bf16 v[16:19], v[84:87], v[76:79], v[16:19]
	ds_read_b128 v[84:87], v0 offset:14336
	s_waitcnt lgkmcnt(2)
	v_mfma_f32_16x16x32_bf16 v[44:47], v[72:75], v[68:71], v[44:47]
	v_mfma_f32_16x16x32_bf16 v[12:15], v[72:75], v[76:79], v[12:15]
	s_waitcnt lgkmcnt(1)
	v_mfma_f32_16x16x32_bf16 v[40:43], v[80:83], v[68:71], v[40:43]
	v_mfma_f32_16x16x32_bf16 v[8:11], v[80:83], v[76:79], v[8:11]
	s_waitcnt lgkmcnt(0)
	v_mfma_f32_16x16x32_bf16 v[36:39], v[84:87], v[68:71], v[36:39]
	s_waitcnt vmcnt(0)
	s_addk_i32 s2, 0xfc00
	s_add_i32 s0, s96, s2
	v_mfma_f32_16x16x32_bf16 v[4:7], v[84:87], v[76:79], v[4:7]
	s_add_i32 s3, s3, 1
	v_lshl_add_u64 v[136:137], v[136:137], 0, s[14:15]
	v_lshl_add_u64 v[134:135], v[134:135], 0, s[14:15]
	v_lshl_add_u64 v[132:133], v[132:133], 0, s[12:13]
	v_lshl_add_u64 v[130:131], v[130:131], 0, s[12:13]
	v_add_u32_e32 v201, 64, v201
	s_cmp_lg_u32 s0, 0
	v_add_u32_e32 v200, 16, v200
	s_waitcnt vmcnt(0)
	s_barrier
	s_cbranch_scc0 .LBB0_675

.LBB0_593:
	s_lshl_b32 s0, s33, 14
	s_add_i32 s0, s0, 0
	v_add_u32_e32 v0, s0, v140
	ds_read_b128 v[68:71], v0
	ds_read_b128 v[72:75], v0 offset:4096
	ds_read_b128 v[76:79], v197
	ds_read_b128 v[80:83], v197 offset:4096
	ds_read_b128 v[84:87], v0 offset:8192
	ds_read_b128 v[92:95], v0 offset:12288
	s_waitcnt lgkmcnt(3)
	v_mfma_f32_16x16x32_bf16 v[88:91], v[68:71], v[76:79], 0
	s_waitcnt lgkmcnt(2)
	v_mfma_f32_16x16x32_bf16 v[68:71], v[68:71], v[80:83], 0
	v_add_u32_e32 v0, s0, v143
	ds_read_b128 v[202:205], v0
	ds_read_b128 v[206:209], v197 offset:1024
	ds_read_b128 v[210:213], v197 offset:5120
	v_mfma_f32_16x16x32_bf16 v[96:99], v[72:75], v[76:79], 0
	v_mfma_f32_16x16x32_bf16 v[72:75], v[72:75], v[80:83], 0
	s_waitcnt lgkmcnt(4)
	v_mfma_f32_16x16x32_bf16 v[214:217], v[84:87], v[76:79], 0
	ds_read_b128 v[218:221], v0 offset:4096
	v_mfma_f32_16x16x32_bf16 v[84:87], v[84:87], v[80:83], 0
	s_waitcnt lgkmcnt(4)
	v_mfma_f32_16x16x32_bf16 v[76:79], v[92:95], v[76:79], 0
	v_mfma_f32_16x16x32_bf16 v[80:83], v[92:95], v[80:83], 0
	ds_read_b128 v[92:95], v0 offset:8192
	s_waitcnt lgkmcnt(3)
	v_mfma_f32_16x16x32_bf16 v[88:91], v[202:205], v[206:209], v[88:91]
	s_waitcnt lgkmcnt(2)
	v_mfma_f32_16x16x32_bf16 v[68:71], v[202:205], v[210:213], v[68:71]
	ds_read_b128 v[202:205], v0 offset:12288
	v_add_u32_e32 v0, s0, v144
	s_waitcnt lgkmcnt(2)
	v_mfma_f32_16x16x32_bf16 v[96:99], v[218:221], v[206:209], v[96:99]
	v_mfma_f32_16x16x32_bf16 v[72:75], v[218:221], v[210:213], v[72:75]
	ds_read_b128 v[218:221], v0
	ds_read_b128 v[222:225], v197 offset:2048
	ds_read_b128 v[228:231], v197 offset:6144
	s_waitcnt lgkmcnt(4)
	v_mfma_f32_16x16x32_bf16 v[214:217], v[92:95], v[206:209], v[214:217]
	v_mfma_f32_16x16x32_bf16 v[84:87], v[92:95], v[210:213], v[84:87]
	ds_read_b128 v[92:95], v0 offset:4096
	s_waitcnt lgkmcnt(4)
	v_mfma_f32_16x16x32_bf16 v[76:79], v[202:205], v[206:209], v[76:79]
	ds_read_b128 v[206:209], v0 offset:8192
	v_mfma_f32_16x16x32_bf16 v[80:83], v[202:205], v[210:213], v[80:83]
	ds_read_b128 v[202:205], v0 offset:12288
	s_waitcnt lgkmcnt(4)
	v_mfma_f32_16x16x32_bf16 v[88:91], v[218:221], v[222:225], v[88:91]
	s_waitcnt lgkmcnt(3)
	v_mfma_f32_16x16x32_bf16 v[68:71], v[218:221], v[228:231], v[68:71]
	v_add_u32_e32 v0, s0, v145
	s_waitcnt lgkmcnt(2)
	v_mfma_f32_16x16x32_bf16 v[210:213], v[92:95], v[222:225], v[96:99]
	v_mfma_f32_16x16x32_bf16 v[72:75], v[92:95], v[228:231], v[72:75]
	ds_read_b128 v[92:95], v0
	ds_read_b128 v[218:221], v197 offset:3072
	ds_read_b128 v[232:235], v197 offset:7168
	s_waitcnt lgkmcnt(4)
	v_mfma_f32_16x16x32_bf16 v[214:217], v[206:209], v[222:225], v[214:217]
	v_mfma_f32_16x16x32_bf16 v[84:87], v[206:209], v[228:231], v[84:87]
	ds_read_b128 v[206:209], v0 offset:4096
	s_waitcnt lgkmcnt(4)
	v_mfma_f32_16x16x32_bf16 v[222:225], v[202:205], v[222:225], v[76:79]
	ds_read_b128 v[236:239], v0 offset:8192
	v_mfma_f32_16x16x32_bf16 v[202:205], v[202:205], v[228:231], v[80:83]
	s_waitcnt lgkmcnt(2)
	v_mfma_f32_16x16x32_bf16 v[80:83], v[92:95], v[232:235], v[68:71]
	s_nop 2
	ds_read_b128 v[68:71], v0 offset:12288
	v_mfma_f32_16x16x32_bf16 v[96:99], v[92:95], v[218:221], v[88:91]
	s_waitcnt lgkmcnt(2)
	v_mfma_f32_16x16x32_bf16 v[92:95], v[206:209], v[218:221], v[210:213]
	v_mfma_f32_16x16x32_bf16 v[76:79], v[206:209], v[232:235], v[72:75]
	s_waitcnt lgkmcnt(1)
	v_mfma_f32_16x16x32_bf16 v[88:91], v[236:239], v[218:221], v[214:217]
	v_mfma_f32_16x16x32_bf16 v[72:75], v[236:239], v[232:235], v[84:87]
	s_waitcnt lgkmcnt(0)
	v_mfma_f32_16x16x32_bf16 v[84:87], v[68:71], v[218:221], v[222:225]
	v_mfma_f32_16x16x32_bf16 v[68:71], v[68:71], v[232:235], v[202:205]
	s_nop 2
	v_add_u32_e32 v204, s2, v195
	v_subrev_u32_e32 v205, 31, v204
	v_cmp_lt_i32_e32 vcc, -1, v205
	v_mov_b32_e32 v202, 0xff800000
	v_mov_b32_e32 v203, 0xff800000
	s_and_saveexec_b64 s[0:1], vcc
	s_cbranch_execz .LBB0_595
	v_min_u32_e32 v0, 0x7f, v205
	v_lshl_add_u32 v0, v0, 2, v196
	ds_read_b32 v203, v0
	s_waitcnt lgkmcnt(0)
	v_fmac_f32_e32 v203, 0x3fb8aa3b, v96

.LBB0_661:
	s_waitcnt lgkmcnt(0)
	s_or_b64 exec, exec, s[0:1]
	v_sub_f32_e32 v0, v95, v198
	v_exp_f32_e32 v68, v0
	v_sub_f32_e32 v0, v94, v198
	v_exp_f32_e32 v69, v0
	v_sub_f32_e32 v0, v89, v198
	v_exp_f32_e32 v70, v0
	v_sub_f32_e32 v0, v88, v198
	v_exp_f32_e32 v71, v0
	v_pk_mul_f32 v[68:69], v[100:101], v[68:69]
	v_pk_mul_f32 v[70:71], v[100:101], v[70:71]
	s_nop 0
	v_add_f32_e32 v0, v70, v71
	v_add_f32_e32 v76, v68, v69
	v_add_f32_e32 v0, v76, v0
	v_add_f32_dpp v78, v71, v71 quad_perm:[1,0,3,2] row_mask:0xf bank_mask:0xf bound_ctrl:1
	s_nop 0
	v_add_f32_dpp v76, v0, v0 quad_perm:[1,0,3,2] row_mask:0xf bank_mask:0xf bound_ctrl:1
	v_mov_b32_dpp v79, v78 quad_perm:[2,3,0,1] row_mask:0xf bank_mask:0xf bound_ctrl:1
	s_nop 0
	v_mov_b32_dpp v77, v76 quad_perm:[2,3,0,1] row_mask:0xf bank_mask:0xf bound_ctrl:1
	s_and_saveexec_b64 s[0:1], s[6:7]
	s_cbranch_execz .LBB0_663
	v_add_f32_e32 v76, v76, v77
	v_add_f32_e32 v0, v78, v79
	s_waitcnt vmcnt(0)
	ds_add_f32 v201, v76 offset:32
	ds_add_f32 v201, v0 offset:36

.LBB0_666:
	s_waitcnt lgkmcnt(0)
	s_or_b64 exec, exec, s[0:1]
	v_sub_f32_e32 v0, v87, v199
	v_exp_f32_e32 v84, v0
	v_sub_f32_e32 v0, v86, v199
	v_exp_f32_e32 v85, v0
	v_sub_f32_e32 v0, v206, v199
	v_exp_f32_e32 v86, v0
	v_sub_f32_e32 v0, v205, v199
	v_exp_f32_e32 v87, v0
	v_pk_mul_f32 v[88:89], v[128:129], v[84:85]
	v_pk_mul_f32 v[90:91], v[128:129], v[86:87]
	s_nop 0
	v_add_f32_e32 v0, v90, v91
	v_add_f32_e32 v84, v88, v89
	v_add_f32_e32 v0, v84, v0
	v_add_f32_dpp v86, v91, v91 quad_perm:[1,0,3,2] row_mask:0xf bank_mask:0xf bound_ctrl:1
	s_nop 0
	v_add_f32_dpp v84, v0, v0 quad_perm:[1,0,3,2] row_mask:0xf bank_mask:0xf bound_ctrl:1
	v_mov_b32_dpp v87, v86 quad_perm:[2,3,0,1] row_mask:0xf bank_mask:0xf bound_ctrl:1
	s_nop 0
	v_mov_b32_dpp v85, v84 quad_perm:[2,3,0,1] row_mask:0xf bank_mask:0xf bound_ctrl:1
	s_and_saveexec_b64 s[0:1], s[6:7]
	s_cbranch_execz .LBB0_668
	v_add_f32_e32 v84, v84, v85
	v_add_f32_e32 v0, v86, v87
	s_waitcnt vmcnt(0)
	ds_add_f32 v201, v84 offset:1024
	ds_add_f32 v201, v0 offset:1028

.LBB0_670:
	s_waitcnt lgkmcnt(0)
	s_or_b64 exec, exec, s[0:1]
	v_sub_f32_e32 v0, v212, v199
	v_exp_f32_e32 v84, v0
	v_sub_f32_e32 v0, v211, v199
	v_exp_f32_e32 v85, v0
	v_sub_f32_e32 v0, v214, v199
	v_exp_f32_e32 v86, v0
	v_sub_f32_e32 v0, v213, v199
	v_exp_f32_e32 v87, v0
	v_pk_mul_f32 v[84:85], v[128:129], v[84:85]
	v_pk_mul_f32 v[86:87], v[128:129], v[86:87]
	s_nop 0
	v_add_f32_e32 v0, v86, v87
	v_add_f32_e32 v92, v84, v85
	v_add_f32_e32 v0, v92, v0
	v_add_f32_dpp v94, v87, v87 quad_perm:[1,0,3,2] row_mask:0xf bank_mask:0xf bound_ctrl:1
	s_nop 0
	v_add_f32_dpp v92, v0, v0 quad_perm:[1,0,3,2] row_mask:0xf bank_mask:0xf bound_ctrl:1
	v_mov_b32_dpp v95, v94 quad_perm:[2,3,0,1] row_mask:0xf bank_mask:0xf bound_ctrl:1
	s_nop 0
	v_mov_b32_dpp v93, v92 quad_perm:[2,3,0,1] row_mask:0xf bank_mask:0xf bound_ctrl:1
	s_and_saveexec_b64 s[0:1], s[6:7]
	s_cbranch_execz .LBB0_672
	v_add_f32_e32 v92, v92, v93
	v_add_f32_e32 v0, v94, v95
	s_waitcnt vmcnt(0)
	ds_add_f32 v201, v92 offset:1056
	ds_add_f32 v201, v0 offset:1060
.LBB0_672:
	s_or_b64 exec, exec, s[0:1]
	v_sub_f32_e32 v0, v216, v199
	v_exp_f32_e32 v92, v0
	v_sub_f32_e32 v0, v215, v199
	v_exp_f32_e32 v93, v0
	v_sub_f32_e32 v0, v218, v199
	v_exp_f32_e32 v94, v0
	v_sub_f32_e32 v0, v217, v199
	v_exp_f32_e32 v95, v0
	v_pk_mul_f32 v[92:93], v[128:129], v[92:93]
	v_pk_mul_f32 v[94:95], v[128:129], v[94:95]
	s_nop 0
	v_add_f32_e32 v0, v94, v95
	v_add_f32_e32 v202, v92, v93
	v_add_f32_e32 v0, v202, v0
	s_nop 0
	v_add_f32_dpp v202, v95, v95 quad_perm:[1,0,3,2] row_mask:0xf bank_mask:0xf bound_ctrl:1
	v_add_f32_dpp v204, v0, v0 quad_perm:[1,0,3,2] row_mask:0xf bank_mask:0xf bound_ctrl:1
	s_nop 0
	v_mov_b32_dpp v203, v202 quad_perm:[2,3,0,1] row_mask:0xf bank_mask:0xf bound_ctrl:1
	v_mov_b32_dpp v205, v204 quad_perm:[2,3,0,1] row_mask:0xf bank_mask:0xf bound_ctrl:1
	s_and_saveexec_b64 s[0:1], s[6:7]
	s_waitcnt lgkmcnt(0)
	s_cbranch_execz .LBB0_590
	v_add_f32_e32 v0, v204, v205
	s_waitcnt vmcnt(0)
	ds_add_f32 v201, v0 offset:1072
	v_cmp_gt_u32_e32 vcc, 63, v200
	s_and_b64 exec, exec, vcc
	s_waitcnt lgkmcnt(0)
	s_cbranch_execz .LBB0_590
	v_add_f32_e32 v0, v202, v203
	ds_add_f32 v201, v0 offset:1076
	s_waitcnt lgkmcnt(0)
	s_branch .LBB0_590
.LBB0_675:
	s_waitcnt lgkmcnt(0)
	s_mov_b32 s8, 0
	v_mov_b32_e32 v68, v155
	s_branch .LBB0_677
	s_nop 0
	s_nop 0
	s_nop 0
	s_nop 0
	s_nop 0

.LBB0_693:
	s_lshl_b32 s0, s83, 14
	s_add_i32 s0, s0, 0
	v_add_u32_e32 v0, s0, v140
	ds_read_b128 v[70:73], v0
	ds_read_b128 v[74:77], v0 offset:4096
	ds_read_b128 v[78:81], v197
	ds_read_b128 v[82:85], v197 offset:4096
	ds_read_b128 v[86:89], v0 offset:8192
	s_add_i32 s1, s37, s33
	s_add_i32 s1, s1, -1
	ds_read_b128 v[94:97], v0 offset:12288
	s_waitcnt lgkmcnt(0)
	v_mfma_f32_16x16x32_bf16 v[90:93], v[70:73], v[78:81], 0
	v_mfma_f32_16x16x32_bf16 v[70:73], v[70:73], v[82:85], 0
	v_add_u32_e32 v0, s0, v143
	ds_read_b128 v[198:201], v0
	ds_read_b128 v[202:205], v197 offset:1024
	ds_read_b128 v[206:209], v197 offset:5120
	v_mfma_f32_16x16x32_bf16 v[98:101], v[74:77], v[78:81], 0
	v_mfma_f32_16x16x32_bf16 v[74:77], v[74:77], v[82:85], 0
	v_mfma_f32_16x16x32_bf16 v[210:213], v[86:89], v[78:81], 0
	ds_read_b128 v[214:217], v0 offset:4096
	v_mfma_f32_16x16x32_bf16 v[86:89], v[86:89], v[82:85], 0
	v_mfma_f32_16x16x32_bf16 v[78:81], v[94:97], v[78:81], 0
	v_mfma_f32_16x16x32_bf16 v[82:85], v[94:97], v[82:85], 0
	ds_read_b128 v[94:97], v0 offset:8192
	s_waitcnt lgkmcnt(3)
	v_mfma_f32_16x16x32_bf16 v[90:93], v[198:201], v[202:205], v[90:93]
	s_waitcnt lgkmcnt(2)
	v_mfma_f32_16x16x32_bf16 v[70:73], v[198:201], v[206:209], v[70:73]
	ds_read_b128 v[198:201], v0 offset:12288
	v_add_u32_e32 v0, s0, v144
	s_waitcnt lgkmcnt(2)
	v_mfma_f32_16x16x32_bf16 v[98:101], v[214:217], v[202:205], v[98:101]
	v_mfma_f32_16x16x32_bf16 v[74:77], v[214:217], v[206:209], v[74:77]
	ds_read_b128 v[214:217], v0
	ds_read_b128 v[218:221], v197 offset:2048
	ds_read_b128 v[222:225], v197 offset:6144
	s_waitcnt lgkmcnt(4)
	v_mfma_f32_16x16x32_bf16 v[210:213], v[94:97], v[202:205], v[210:213]
	v_mfma_f32_16x16x32_bf16 v[86:89], v[94:97], v[206:209], v[86:89]
	ds_read_b128 v[94:97], v0 offset:4096
	s_waitcnt lgkmcnt(4)
	v_mfma_f32_16x16x32_bf16 v[78:81], v[198:201], v[202:205], v[78:81]
	ds_read_b128 v[202:205], v0 offset:8192
	v_mfma_f32_16x16x32_bf16 v[82:85], v[198:201], v[206:209], v[82:85]
	s_waitcnt lgkmcnt(3)
	v_mfma_f32_16x16x32_bf16 v[90:93], v[214:217], v[218:221], v[90:93]
	ds_read_b128 v[198:201], v0 offset:12288
	s_waitcnt lgkmcnt(3)
	v_mfma_f32_16x16x32_bf16 v[70:73], v[214:217], v[222:225], v[70:73]
	v_add_u32_e32 v0, s0, v145
	s_waitcnt lgkmcnt(2)
	v_mfma_f32_16x16x32_bf16 v[206:209], v[94:97], v[218:221], v[98:101]
	v_mfma_f32_16x16x32_bf16 v[74:77], v[94:97], v[222:225], v[74:77]
	ds_read_b128 v[94:97], v0
	ds_read_b128 v[214:217], v197 offset:3072
	ds_read_b128 v[228:231], v197 offset:7168
	s_waitcnt lgkmcnt(4)
	v_mfma_f32_16x16x32_bf16 v[210:213], v[202:205], v[218:221], v[210:213]
	v_mfma_f32_16x16x32_bf16 v[86:89], v[202:205], v[222:225], v[86:89]
	ds_read_b128 v[202:205], v0 offset:4096
	ds_read_b128 v[232:235], v0 offset:8192
	s_waitcnt lgkmcnt(5)
	v_mfma_f32_16x16x32_bf16 v[218:221], v[198:201], v[218:221], v[78:81]
	v_mfma_f32_16x16x32_bf16 v[198:201], v[198:201], v[222:225], v[82:85]
	s_waitcnt lgkmcnt(3)
	v_mfma_f32_16x16x32_bf16 v[82:85], v[94:97], v[214:217], v[90:93]
	ds_read_b128 v[222:225], v0 offset:12288
	s_waitcnt lgkmcnt(3)
	v_mfma_f32_16x16x32_bf16 v[98:101], v[94:97], v[228:231], v[70:73]
	s_waitcnt lgkmcnt(2)
	v_mfma_f32_16x16x32_bf16 v[78:81], v[202:205], v[214:217], v[206:209]
	v_mfma_f32_16x16x32_bf16 v[94:97], v[202:205], v[228:231], v[74:77]
	s_waitcnt lgkmcnt(1)
	v_mfma_f32_16x16x32_bf16 v[74:77], v[232:235], v[214:217], v[210:213]
	v_mfma_f32_16x16x32_bf16 v[90:93], v[232:235], v[228:231], v[86:89]
	s_nop 0
	v_max_f32_e32 v2, v82, v83
	s_waitcnt lgkmcnt(0)
	v_mfma_f32_16x16x32_bf16 v[70:73], v[222:225], v[214:217], v[218:221]
	s_ashr_i32 s22, s1, 5
	v_max_f32_e32 v125, v84, v85
	v_mfma_f32_16x16x32_bf16 v[86:89], v[222:225], v[228:231], v[198:201]
	v_lshl_add_u32 v134, s22, 2, v148
	ds_read_b32 v5, v196 offset:508
	ds_read_b32 v0, v134
	v_max_f32_e32 v137, v80, v81
	v_max3_f32 v137, v78, v79, v137
	v_max3_f32 v2, v2, v125, v137
	v_max_f32_e32 v125, v76, v77
	v_max_f32_e32 v137, v72, v73
	s_lshl_b32 s0, 1, s1
	v_max3_f32 v125, v74, v75, v125
	v_max3_f32 v137, v70, v71, v137
	s_waitcnt lgkmcnt(0)
	v_and_b32_e32 v0, s0, v0
	v_max3_f32 v2, v2, v125, v137
	v_cmp_ne_u32_e32 vcc, 0, v0
	v_mov_b32_e32 v0, v2
	s_nop 1
	v_permlane16_swap_b32_e32 v2, v0
	v_max_f32_e32 v0, v2, v0
	v_mov_b32_e32 v2, v0
	s_nop 1
	v_permlane32_swap_b32_e32 v0, v2
	v_cndmask_b32_e32 v137, v159, v5, vcc
	v_max_f32_e32 v0, v0, v2
	v_fmamk_f32 v0, v0, 0x3fb8aa3b, v137
	v_max_f32_e32 v125, v133, v0
	v_sub_f32_e32 v0, v133, v125
	v_exp_f32_e32 v2, v0
	s_nop 0
	v_cmp_neq_f32_e32 vcc, 1.0, v2
	s_cbranch_vccz .LBB0_695
	v_pk_mul_f32 v[68:69], v[68:69], v[2:3] op_sel_hi:[1,0]
	v_pk_mul_f32 v[66:67], v[66:67], v[2:3] op_sel_hi:[1,0]
	v_pk_mul_f32 v[64:65], v[64:65], v[2:3] op_sel_hi:[1,0]
	v_pk_mul_f32 v[62:63], v[62:63], v[2:3] op_sel_hi:[1,0]
	v_pk_mul_f32 v[60:61], v[60:61], v[2:3] op_sel_hi:[1,0]
	v_pk_mul_f32 v[58:59], v[58:59], v[2:3] op_sel_hi:[1,0]
	v_pk_mul_f32 v[56:57], v[56:57], v[2:3] op_sel_hi:[1,0]
	v_pk_mul_f32 v[54:55], v[54:55], v[2:3] op_sel_hi:[1,0]
	v_pk_mul_f32 v[52:53], v[52:53], v[2:3] op_sel_hi:[1,0]
	v_pk_mul_f32 v[50:51], v[50:51], v[2:3] op_sel_hi:[1,0]
	v_pk_mul_f32 v[48:49], v[48:49], v[2:3] op_sel_hi:[1,0]
	v_pk_mul_f32 v[46:47], v[46:47], v[2:3] op_sel_hi:[1,0]
	v_pk_mul_f32 v[44:45], v[44:45], v[2:3] op_sel_hi:[1,0]
	v_pk_mul_f32 v[42:43], v[42:43], v[2:3] op_sel_hi:[1,0]
	v_pk_mul_f32 v[40:41], v[40:41], v[2:3] op_sel_hi:[1,0]
	v_pk_mul_f32 v[38:39], v[38:39], v[2:3] op_sel_hi:[1,0]
.LBB0_695:
	ds_read_b32 v0, v134 offset:32
	v_max_f32_e32 v133, v98, v99
	v_max_f32_e32 v134, v100, v101
	v_max_f32_e32 v198, v96, v97
	v_max3_f32 v198, v94, v95, v198
	v_max3_f32 v133, v133, v134, v198
	v_max_f32_e32 v134, v92, v93
	v_max_f32_e32 v198, v88, v89
	v_max3_f32 v134, v90, v91, v134
	v_max3_f32 v198, v86, v87, v198
	s_waitcnt lgkmcnt(0)
	v_and_b32_e32 v0, s0, v0
	v_max3_f32 v133, v133, v134, v198
	v_cmp_ne_u32_e32 vcc, 0, v0
	v_mov_b32_e32 v0, v133
	s_nop 1
	v_permlane16_swap_b32_e32 v133, v0
	v_max_f32_e32 v0, v133, v0
	v_mov_b32_e32 v133, v0
	s_nop 1
	v_permlane32_swap_b32_e32 v0, v133
	v_cndmask_b32_e32 v5, v159, v5, vcc
	v_max_f32_e32 v0, v0, v133
	v_fmamk_f32 v0, v0, 0x3fb8aa3b, v5
	v_max_f32_e32 v134, v4, v0
	v_sub_f32_e32 v0, v4, v134
	v_exp_f32_e32 v4, v0
	s_nop 0
	v_cmp_neq_f32_e32 vcc, 1.0, v4
	s_cbranch_vccz .LBB0_697
	v_pk_mul_f32 v[36:37], v[36:37], v[4:5] op_sel_hi:[1,0]
	v_pk_mul_f32 v[34:35], v[34:35], v[4:5] op_sel_hi:[1,0]
	v_pk_mul_f32 v[32:33], v[32:33], v[4:5] op_sel_hi:[1,0]
	v_pk_mul_f32 v[30:31], v[30:31], v[4:5] op_sel_hi:[1,0]
	v_pk_mul_f32 v[28:29], v[28:29], v[4:5] op_sel_hi:[1,0]
	v_pk_mul_f32 v[26:27], v[26:27], v[4:5] op_sel_hi:[1,0]
	v_pk_mul_f32 v[24:25], v[24:25], v[4:5] op_sel_hi:[1,0]
	v_pk_mul_f32 v[22:23], v[22:23], v[4:5] op_sel_hi:[1,0]
	v_pk_mul_f32 v[20:21], v[20:21], v[4:5] op_sel_hi:[1,0]
	v_pk_mul_f32 v[18:19], v[18:19], v[4:5] op_sel_hi:[1,0]
	v_pk_mul_f32 v[16:17], v[16:17], v[4:5] op_sel_hi:[1,0]
	v_pk_mul_f32 v[14:15], v[14:15], v[4:5] op_sel_hi:[1,0]
	v_pk_mul_f32 v[12:13], v[12:13], v[4:5] op_sel_hi:[1,0]
	v_pk_mul_f32 v[10:11], v[10:11], v[4:5] op_sel_hi:[1,0]
	v_pk_mul_f32 v[8:9], v[8:9], v[4:5] op_sel_hi:[1,0]
	v_pk_mul_f32 v[6:7], v[6:7], v[4:5] op_sel_hi:[1,0]
.LBB0_697:
	v_sub_f32_e32 v0, v5, v134
	v_fmamk_f32 v5, v98, 0x3fb8aa3b, v0
	v_exp_f32_e32 v98, v5
	v_fmamk_f32 v5, v99, 0x3fb8aa3b, v0
	v_exp_f32_e32 v99, v5
	v_fmamk_f32 v5, v100, 0x3fb8aa3b, v0
	v_exp_f32_e32 v100, v5
	v_fmamk_f32 v5, v101, 0x3fb8aa3b, v0
	v_exp_f32_e32 v101, v5
	v_fmamk_f32 v94, v94, 0x3fb8aa3b, v0
	v_add_f32_e32 v5, 0, v98
	v_exp_f32_e32 v94, v94
	v_fmamk_f32 v95, v95, 0x3fb8aa3b, v0
	v_add_f32_e32 v5, v99, v5
	v_exp_f32_e32 v95, v95
	v_fmamk_f32 v96, v96, 0x3fb8aa3b, v0
	v_add_f32_e32 v5, v100, v5
	v_exp_f32_e32 v96, v96
	v_fmamk_f32 v97, v97, 0x3fb8aa3b, v0
	v_add_f32_e32 v5, v101, v5
	v_exp_f32_e32 v97, v97
	v_fmamk_f32 v90, v90, 0x3fb8aa3b, v0
	v_add_f32_e32 v5, v94, v5
	v_exp_f32_e32 v90, v90
	v_fmamk_f32 v91, v91, 0x3fb8aa3b, v0
	v_add_f32_e32 v5, v95, v5
	v_exp_f32_e32 v91, v91
	v_fmamk_f32 v92, v92, 0x3fb8aa3b, v0
	v_add_f32_e32 v5, v96, v5
	v_exp_f32_e32 v92, v92
	v_fmamk_f32 v93, v93, 0x3fb8aa3b, v0
	v_add_f32_e32 v5, v97, v5
	v_exp_f32_e32 v93, v93
	v_fmamk_f32 v86, v86, 0x3fb8aa3b, v0
	v_add_f32_e32 v5, v90, v5
	v_exp_f32_e32 v198, v86
	v_fmamk_f32 v86, v87, 0x3fb8aa3b, v0
	v_add_f32_e32 v5, v91, v5
	v_exp_f32_e32 v199, v86
	v_fmamk_f32 v86, v88, 0x3fb8aa3b, v0
	v_add_f32_e32 v5, v92, v5
	v_exp_f32_e32 v200, v86
	v_fmac_f32_e32 v0, 0x3fb8aa3b, v89
	v_add_f32_e32 v5, v93, v5
	v_exp_f32_e32 v0, v0
	v_add_f32_e32 v5, v198, v5
	v_add_f32_e32 v5, v199, v5
	v_add_f32_e32 v5, v200, v5
	v_add_f32_e32 v5, v0, v5
	v_fmac_f32_e32 v5, v136, v4
	v_sub_f32_e32 v4, v137, v125
	v_fmamk_f32 v82, v82, 0x3fb8aa3b, v4
	v_exp_f32_e32 v82, v82
	v_fmamk_f32 v83, v83, 0x3fb8aa3b, v4
	v_exp_f32_e32 v83, v83
	v_fmamk_f32 v84, v84, 0x3fb8aa3b, v4
	v_exp_f32_e32 v84, v84
	v_fmamk_f32 v85, v85, 0x3fb8aa3b, v4
	v_exp_f32_e32 v85, v85
	v_fmamk_f32 v78, v78, 0x3fb8aa3b, v4
	v_add_f32_e32 v86, 0, v82
	v_exp_f32_e32 v87, v78
	v_fmamk_f32 v78, v79, 0x3fb8aa3b, v4
	v_add_f32_e32 v86, v83, v86
	v_exp_f32_e32 v88, v78
	v_fmamk_f32 v78, v80, 0x3fb8aa3b, v4
	v_add_f32_e32 v86, v84, v86
	v_exp_f32_e32 v89, v78
	v_fmamk_f32 v78, v81, 0x3fb8aa3b, v4
	v_add_f32_e32 v86, v85, v86
	v_exp_f32_e32 v81, v78
	v_fmamk_f32 v74, v74, 0x3fb8aa3b, v4
	v_add_f32_e32 v78, v87, v86
	v_exp_f32_e32 v136, v74
	v_fmamk_f32 v74, v75, 0x3fb8aa3b, v4
	v_add_f32_e32 v78, v88, v78
	v_exp_f32_e32 v137, v74
	v_fmamk_f32 v74, v76, 0x3fb8aa3b, v4
	v_add_f32_e32 v78, v89, v78
	v_exp_f32_e32 v201, v74
	v_fmamk_f32 v74, v77, 0x3fb8aa3b, v4
	v_add_f32_e32 v78, v81, v78
	v_exp_f32_e32 v202, v74
	v_fmamk_f32 v70, v70, 0x3fb8aa3b, v4
	v_add_f32_e32 v74, v136, v78
	v_exp_f32_e32 v203, v70
	v_fmamk_f32 v70, v71, 0x3fb8aa3b, v4
	v_add_f32_e32 v74, v137, v74
	v_exp_f32_e32 v204, v70
	v_fmamk_f32 v70, v72, 0x3fb8aa3b, v4
	v_add_f32_e32 v74, v201, v74
	v_exp_f32_e32 v205, v70
	v_fmac_f32_e32 v4, 0x3fb8aa3b, v73
	v_add_f32_e32 v74, v202, v74
	v_exp_f32_e32 v4, v4
	v_add_f32_e32 v70, v203, v74
	s_cmp_eq_u32 s83, 0
	v_add_f32_e32 v70, v204, v70
	v_add_f32_e32 v70, v205, v70
	s_cselect_b32 s0, 0x8000, s79
	v_add_f32_e32 v133, v4, v70
	s_add_i32 s0, s0, 0
	v_fmac_f32_e32 v133, v135, v2
	v_add_u32_e32 v2, s0, v142
	ds_read_b128 v[70:73], v2
	ds_read_b128 v[74:77], v2 offset:2048
	v_cvt_pk_bf16_f32 v78, v82, v83
	v_cvt_pk_bf16_f32 v79, v84, v85
	ds_read_b128 v[82:85], v2 offset:4096
	v_cvt_pk_bf16_f32 v80, v87, v88
	v_cvt_pk_bf16_f32 v81, v89, v81
	v_cvt_pk_bf16_f32 v86, v98, v99
	v_cvt_pk_bf16_f32 v87, v100, v101
	v_cvt_pk_bf16_f32 v88, v94, v95
	v_cvt_pk_bf16_f32 v89, v96, v97
	s_waitcnt lgkmcnt(2)
	v_mfma_f32_16x16x32_bf16 v[66:69], v[70:73], v[78:81], v[66:69]
	v_mfma_f32_16x16x32_bf16 v[34:37], v[70:73], v[86:89], v[34:37]
	ds_read_b128 v[70:73], v2 offset:6144
	s_waitcnt lgkmcnt(2)
	v_mfma_f32_16x16x32_bf16 v[62:65], v[74:77], v[78:81], v[62:65]
	v_mfma_f32_16x16x32_bf16 v[30:33], v[74:77], v[86:89], v[30:33]
	ds_read_b128 v[74:77], v2 offset:8192
	s_waitcnt lgkmcnt(2)
	v_mfma_f32_16x16x32_bf16 v[58:61], v[82:85], v[78:81], v[58:61]
	v_mfma_f32_16x16x32_bf16 v[26:29], v[82:85], v[86:89], v[26:29]
	ds_read_b128 v[82:85], v2 offset:10240
	s_waitcnt lgkmcnt(2)
	v_mfma_f32_16x16x32_bf16 v[54:57], v[70:73], v[78:81], v[54:57]
	v_mfma_f32_16x16x32_bf16 v[22:25], v[70:73], v[86:89], v[22:25]
	ds_read_b128 v[70:73], v2 offset:12288
	s_waitcnt lgkmcnt(2)
	v_mfma_f32_16x16x32_bf16 v[50:53], v[74:77], v[78:81], v[50:53]
	v_mfma_f32_16x16x32_bf16 v[18:21], v[74:77], v[86:89], v[18:21]
	ds_read_b128 v[74:77], v2 offset:14336
	v_add_u32_e32 v2, s0, v146
	s_waitcnt lgkmcnt(2)
	v_mfma_f32_16x16x32_bf16 v[46:49], v[82:85], v[78:81], v[46:49]
	v_mfma_f32_16x16x32_bf16 v[14:17], v[82:85], v[86:89], v[14:17]
	ds_read_b128 v[82:85], v2
	s_waitcnt lgkmcnt(2)
	v_mfma_f32_16x16x32_bf16 v[42:45], v[70:73], v[78:81], v[42:45]
	v_mfma_f32_16x16x32_bf16 v[10:13], v[70:73], v[86:89], v[10:13]
	ds_read_b128 v[70:73], v2 offset:2048
	s_waitcnt lgkmcnt(2)
	v_mfma_f32_16x16x32_bf16 v[38:41], v[74:77], v[78:81], v[38:41]
	v_cvt_pk_bf16_f32 v78, v90, v91
	v_cvt_pk_bf16_f32 v79, v92, v93
	v_cvt_pk_bf16_f32 v80, v198, v199
	v_mfma_f32_16x16x32_bf16 v[6:9], v[74:77], v[86:89], v[6:9]
	ds_read_b128 v[86:89], v2 offset:4096
	v_cvt_pk_bf16_f32 v74, v136, v137
	v_cvt_pk_bf16_f32 v75, v201, v202
	v_cvt_pk_bf16_f32 v76, v203, v204
	v_cvt_pk_bf16_f32 v77, v205, v4
	v_cvt_pk_bf16_f32 v81, v200, v0
	s_nop 0
	s_waitcnt lgkmcnt(2)
	v_mfma_f32_16x16x32_bf16 v[66:69], v[82:85], v[74:77], v[66:69]
	v_mfma_f32_16x16x32_bf16 v[34:37], v[82:85], v[78:81], v[34:37]
	ds_read_b128 v[82:85], v2 offset:6144
	s_waitcnt lgkmcnt(2)
	v_mfma_f32_16x16x32_bf16 v[62:65], v[70:73], v[74:77], v[62:65]
	v_mfma_f32_16x16x32_bf16 v[30:33], v[70:73], v[78:81], v[30:33]
	ds_read_b128 v[70:73], v2 offset:8192
	s_waitcnt lgkmcnt(2)
	v_mfma_f32_16x16x32_bf16 v[58:61], v[86:89], v[74:77], v[58:61]
	v_mfma_f32_16x16x32_bf16 v[26:29], v[86:89], v[78:81], v[26:29]
	ds_read_b128 v[86:89], v2 offset:10240
	s_waitcnt lgkmcnt(2)
	v_mfma_f32_16x16x32_bf16 v[54:57], v[82:85], v[74:77], v[54:57]
	v_mfma_f32_16x16x32_bf16 v[22:25], v[82:85], v[78:81], v[22:25]
	ds_read_b128 v[82:85], v2 offset:12288
	s_waitcnt lgkmcnt(2)
	v_mfma_f32_16x16x32_bf16 v[50:53], v[70:73], v[74:77], v[50:53]
	v_mfma_f32_16x16x32_bf16 v[18:21], v[70:73], v[78:81], v[18:21]
	ds_read_b128 v[70:73], v2 offset:14336
	s_waitcnt lgkmcnt(2)
	v_mfma_f32_16x16x32_bf16 v[46:49], v[86:89], v[74:77], v[46:49]
	v_mfma_f32_16x16x32_bf16 v[14:17], v[86:89], v[78:81], v[14:17]
	s_waitcnt lgkmcnt(1)
	v_mfma_f32_16x16x32_bf16 v[42:45], v[82:85], v[74:77], v[42:45]
	v_mfma_f32_16x16x32_bf16 v[10:13], v[82:85], v[78:81], v[10:13]
	s_waitcnt lgkmcnt(0)
	v_mfma_f32_16x16x32_bf16 v[38:41], v[70:73], v[74:77], v[38:41]
	s_waitcnt vmcnt(0)
	s_add_i32 s33, s33, 1
	s_add_i32 s0, s8, s33
	v_mfma_f32_16x16x32_bf16 v[6:9], v[70:73], v[78:81], v[6:9]
	s_cmp_eq_u32 s0, 1
	s_waitcnt vmcnt(0)
	s_barrier
	s_cbranch_scc1 .LBB0_700
	v_mov_b32_e32 v136, v5
	v_mov_b32_e32 v135, v133
	v_mov_b32_e32 v133, v125
	v_mov_b32_e32 v4, v134
	s_branch .LBB0_687

.LBB0_700:
	s_lshl_b32 s8, s36, 19
	s_cmp_gt_i32 s82, s86
	s_cbranch_scc1 .LBB0_781
	s_sub_i32 s36, s2, s43
	s_sub_i32 s84, 0, s42
	s_cmp_ge_i32 s82, s42
	s_mov_b64 s[0:1], -1
	s_cbranch_scc0 .LBB0_704
	s_branch .LBB0_703
	s_nop 0
	s_nop 0
	s_nop 0
	s_nop 0
	s_nop 0
	s_nop 0
	s_nop 0
	s_nop 0
	s_nop 0

.LBB0_712:
	s_lshl_b32 s0, s83, 14
	s_add_i32 s0, s0, 0
	v_add_u32_e32 v0, s0, v140
	ds_read_b128 v[70:73], v0
	ds_read_b128 v[74:77], v0 offset:4096
	ds_read_b128 v[78:81], v197
	ds_read_b128 v[82:85], v197 offset:4096
	ds_read_b128 v[86:89], v0 offset:8192
	ds_read_b128 v[94:97], v0 offset:12288
	s_waitcnt lgkmcnt(0)
	v_mfma_f32_16x16x32_bf16 v[90:93], v[70:73], v[78:81], 0
	v_mfma_f32_16x16x32_bf16 v[70:73], v[70:73], v[82:85], 0
	v_add_u32_e32 v0, s0, v143
	ds_read_b128 v[198:201], v0
	ds_read_b128 v[202:205], v197 offset:1024
	ds_read_b128 v[206:209], v197 offset:5120
	v_mfma_f32_16x16x32_bf16 v[98:101], v[74:77], v[78:81], 0
	v_mfma_f32_16x16x32_bf16 v[74:77], v[74:77], v[82:85], 0
	v_mfma_f32_16x16x32_bf16 v[210:213], v[86:89], v[78:81], 0
	ds_read_b128 v[214:217], v0 offset:4096
	v_mfma_f32_16x16x32_bf16 v[86:89], v[86:89], v[82:85], 0
	v_mfma_f32_16x16x32_bf16 v[78:81], v[94:97], v[78:81], 0
	v_mfma_f32_16x16x32_bf16 v[82:85], v[94:97], v[82:85], 0
	ds_read_b128 v[94:97], v0 offset:8192
	s_waitcnt lgkmcnt(3)
	v_mfma_f32_16x16x32_bf16 v[90:93], v[198:201], v[202:205], v[90:93]
	s_waitcnt lgkmcnt(2)
	v_mfma_f32_16x16x32_bf16 v[70:73], v[198:201], v[206:209], v[70:73]
	ds_read_b128 v[198:201], v0 offset:12288
	v_add_u32_e32 v0, s0, v144
	s_waitcnt lgkmcnt(2)
	v_mfma_f32_16x16x32_bf16 v[98:101], v[214:217], v[202:205], v[98:101]
	v_mfma_f32_16x16x32_bf16 v[74:77], v[214:217], v[206:209], v[74:77]
	ds_read_b128 v[214:217], v0
	ds_read_b128 v[218:221], v197 offset:2048
	ds_read_b128 v[222:225], v197 offset:6144
	s_waitcnt lgkmcnt(4)
	v_mfma_f32_16x16x32_bf16 v[210:213], v[94:97], v[202:205], v[210:213]
	v_mfma_f32_16x16x32_bf16 v[86:89], v[94:97], v[206:209], v[86:89]
	ds_read_b128 v[94:97], v0 offset:4096
	s_waitcnt lgkmcnt(4)
	v_mfma_f32_16x16x32_bf16 v[78:81], v[198:201], v[202:205], v[78:81]
	ds_read_b128 v[202:205], v0 offset:8192
	v_mfma_f32_16x16x32_bf16 v[82:85], v[198:201], v[206:209], v[82:85]
	s_waitcnt lgkmcnt(3)
	v_mfma_f32_16x16x32_bf16 v[90:93], v[214:217], v[218:221], v[90:93]
	ds_read_b128 v[198:201], v0 offset:12288
	s_waitcnt lgkmcnt(3)
	v_mfma_f32_16x16x32_bf16 v[70:73], v[214:217], v[222:225], v[70:73]
	v_add_u32_e32 v0, s0, v145
	s_waitcnt lgkmcnt(2)
	v_mfma_f32_16x16x32_bf16 v[206:209], v[94:97], v[218:221], v[98:101]
	v_mfma_f32_16x16x32_bf16 v[74:77], v[94:97], v[222:225], v[74:77]
	ds_read_b128 v[94:97], v0
	ds_read_b128 v[214:217], v197 offset:3072
	ds_read_b128 v[228:231], v197 offset:7168
	s_waitcnt lgkmcnt(4)
	v_mfma_f32_16x16x32_bf16 v[210:213], v[202:205], v[218:221], v[210:213]
	v_mfma_f32_16x16x32_bf16 v[86:89], v[202:205], v[222:225], v[86:89]
	ds_read_b128 v[202:205], v0 offset:4096
	ds_read_b128 v[232:235], v0 offset:8192
	s_waitcnt lgkmcnt(5)
	v_mfma_f32_16x16x32_bf16 v[218:221], v[198:201], v[218:221], v[78:81]
	v_mfma_f32_16x16x32_bf16 v[198:201], v[198:201], v[222:225], v[82:85]
	s_waitcnt lgkmcnt(2)
	v_mfma_f32_16x16x32_bf16 v[82:85], v[94:97], v[228:231], v[70:73]
	s_nop 2
	ds_read_b128 v[70:73], v0 offset:12288
	v_mfma_f32_16x16x32_bf16 v[98:101], v[94:97], v[214:217], v[90:93]
	s_waitcnt lgkmcnt(2)
	v_mfma_f32_16x16x32_bf16 v[94:97], v[202:205], v[214:217], v[206:209]
	v_mfma_f32_16x16x32_bf16 v[78:81], v[202:205], v[228:231], v[74:77]
	s_waitcnt lgkmcnt(1)
	v_mfma_f32_16x16x32_bf16 v[90:93], v[232:235], v[214:217], v[210:213]
	v_mfma_f32_16x16x32_bf16 v[74:77], v[232:235], v[228:231], v[86:89]
	s_ashr_i32 s0, s22, 5
	v_lshl_add_u32 v137, s0, 2, v148
	ds_read_b32 v0, v137
	s_waitcnt lgkmcnt(1)
	v_mfma_f32_16x16x32_bf16 v[86:89], v[70:73], v[214:217], v[218:221]
	s_lshl_b32 s82, 1, s22
	v_lshl_or_b32 v2, s22, 6, v149
	v_sub_u32_e32 v4, v160, v2
	v_mfma_f32_16x16x32_bf16 v[70:73], v[70:73], v[228:231], v[198:201]
	s_waitcnt lgkmcnt(0)
	v_and_b32_e32 v0, s82, v0
	v_cmp_ne_u32_e32 vcc, 0, v0
	v_cmp_lt_i32_e64 s[0:1], -1, v4
	s_and_b64 s[22:23], vcc, s[0:1]
	v_mov_b32_e32 v135, 0xff800000
	v_mov_b32_e32 v136, 0xff800000
	s_and_saveexec_b64 s[0:1], s[22:23]
	s_cbranch_execz .LBB0_714
	v_min_u32_e32 v0, 0x7f, v4
	v_lshl_add_u32 v0, v0, 2, v196
	ds_read_b32 v136, v0
	s_waitcnt lgkmcnt(0)
	v_fmac_f32_e32 v136, 0x3fb8aa3b, v98

.LBB0_776:
	s_or_b64 exec, exec, s[0:1]
	v_max_f32_e32 v0, v136, v135
	v_max3_f32 v0, v0, v99, v98
	v_max3_f32 v0, v0, v101, v100
	v_max3_f32 v0, v0, v95, v94
	v_max3_f32 v0, v0, v97, v96
	v_max3_f32 v0, v0, v91, v90
	v_max3_f32 v0, v0, v93, v92
	v_max3_f32 v0, v0, v87, v86
	v_mov_b32_e32 v2, v0
	s_nop 1
	v_permlane16_swap_b32_e32 v0, v2
	v_max_f32_e32 v0, v0, v2
	v_mov_b32_e32 v2, v0
	s_nop 1
	v_permlane32_swap_b32_e32 v0, v2
	v_max3_f32 v71, v125, v0, v2
	v_sub_f32_e32 v0, v125, v71
	v_exp_f32_e32 v2, v0
	s_nop 0
	v_cmp_neq_f32_e32 vcc, 1.0, v2
	s_cbranch_vccz .LBB0_778
	v_pk_mul_f32 v[68:69], v[68:69], v[2:3] op_sel_hi:[1,0]
	v_pk_mul_f32 v[66:67], v[66:67], v[2:3] op_sel_hi:[1,0]
	v_pk_mul_f32 v[64:65], v[64:65], v[2:3] op_sel_hi:[1,0]
	v_pk_mul_f32 v[62:63], v[62:63], v[2:3] op_sel_hi:[1,0]
	v_pk_mul_f32 v[60:61], v[60:61], v[2:3] op_sel_hi:[1,0]
	v_pk_mul_f32 v[58:59], v[58:59], v[2:3] op_sel_hi:[1,0]
	v_pk_mul_f32 v[56:57], v[56:57], v[2:3] op_sel_hi:[1,0]
	v_pk_mul_f32 v[54:55], v[54:55], v[2:3] op_sel_hi:[1,0]
	v_pk_mul_f32 v[52:53], v[52:53], v[2:3] op_sel_hi:[1,0]
	v_pk_mul_f32 v[50:51], v[50:51], v[2:3] op_sel_hi:[1,0]
	v_pk_mul_f32 v[48:49], v[48:49], v[2:3] op_sel_hi:[1,0]
	v_pk_mul_f32 v[46:47], v[46:47], v[2:3] op_sel_hi:[1,0]
	v_pk_mul_f32 v[44:45], v[44:45], v[2:3] op_sel_hi:[1,0]
	v_pk_mul_f32 v[42:43], v[42:43], v[2:3] op_sel_hi:[1,0]
	v_pk_mul_f32 v[40:41], v[40:41], v[2:3] op_sel_hi:[1,0]
	v_pk_mul_f32 v[38:39], v[38:39], v[2:3] op_sel_hi:[1,0]
.LBB0_778:
	v_max_f32_e32 v0, v89, v88
	v_max3_f32 v0, v0, v83, v82
	v_max3_f32 v0, v0, v85, v84
	v_max3_f32 v0, v0, v79, v78
	v_max3_f32 v0, v0, v81, v80
	v_max3_f32 v0, v0, v75, v74
	v_max3_f32 v0, v0, v77, v76
	v_max3_f32 v0, v0, v137, v70
	v_mov_b32_e32 v4, v0
	s_nop 1
	v_permlane16_swap_b32_e32 v0, v4
	v_max_f32_e32 v0, v0, v4
	v_mov_b32_e32 v4, v0
	s_nop 1
	v_permlane32_swap_b32_e32 v0, v4
	v_max3_f32 v72, v134, v0, v4
	v_sub_f32_e32 v0, v134, v72
	v_exp_f32_e32 v4, v0
	s_nop 0
	v_cmp_neq_f32_e32 vcc, 1.0, v4
	s_cbranch_vccz .LBB0_780
	v_pk_mul_f32 v[36:37], v[36:37], v[4:5] op_sel_hi:[1,0]
	v_pk_mul_f32 v[34:35], v[34:35], v[4:5] op_sel_hi:[1,0]
	v_pk_mul_f32 v[32:33], v[32:33], v[4:5] op_sel_hi:[1,0]
	v_pk_mul_f32 v[30:31], v[30:31], v[4:5] op_sel_hi:[1,0]
	v_pk_mul_f32 v[28:29], v[28:29], v[4:5] op_sel_hi:[1,0]
	v_pk_mul_f32 v[26:27], v[26:27], v[4:5] op_sel_hi:[1,0]
	v_pk_mul_f32 v[24:25], v[24:25], v[4:5] op_sel_hi:[1,0]
	v_pk_mul_f32 v[22:23], v[22:23], v[4:5] op_sel_hi:[1,0]
	v_pk_mul_f32 v[20:21], v[20:21], v[4:5] op_sel_hi:[1,0]
	v_pk_mul_f32 v[18:19], v[18:19], v[4:5] op_sel_hi:[1,0]
	v_pk_mul_f32 v[16:17], v[16:17], v[4:5] op_sel_hi:[1,0]
	v_pk_mul_f32 v[14:15], v[14:15], v[4:5] op_sel_hi:[1,0]
	v_pk_mul_f32 v[12:13], v[12:13], v[4:5] op_sel_hi:[1,0]
	v_pk_mul_f32 v[10:11], v[10:11], v[4:5] op_sel_hi:[1,0]
	v_pk_mul_f32 v[8:9], v[8:9], v[4:5] op_sel_hi:[1,0]
	v_pk_mul_f32 v[6:7], v[6:7], v[4:5] op_sel_hi:[1,0]
.LBB0_780:
	v_sub_f32_e32 v0, v89, v72
	v_exp_f32_e32 v0, v0
	v_sub_f32_e32 v73, v88, v72
	v_exp_f32_e32 v73, v73
	v_sub_f32_e32 v83, v83, v72
	v_exp_f32_e32 v125, v83
	v_sub_f32_e32 v82, v82, v72
	v_exp_f32_e32 v134, v82
	v_sub_f32_e32 v83, v85, v72
	v_add_f32_e32 v82, 0, v0
	v_exp_f32_e32 v198, v83
	v_sub_f32_e32 v83, v84, v72
	v_add_f32_e32 v82, v73, v82
	v_exp_f32_e32 v199, v83
	v_sub_f32_e32 v79, v79, v72
	v_add_f32_e32 v82, v125, v82
	v_exp_f32_e32 v200, v79
	v_sub_f32_e32 v78, v78, v72
	v_add_f32_e32 v82, v134, v82
	v_exp_f32_e32 v201, v78
	v_sub_f32_e32 v79, v81, v72
	v_add_f32_e32 v78, v198, v82
	v_exp_f32_e32 v202, v79
	v_sub_f32_e32 v79, v80, v72
	v_add_f32_e32 v78, v199, v78
	v_exp_f32_e32 v203, v79
	v_sub_f32_e32 v75, v75, v72
	v_add_f32_e32 v78, v200, v78
	v_exp_f32_e32 v204, v75
	v_sub_f32_e32 v74, v74, v72
	v_add_f32_e32 v78, v201, v78
	v_exp_f32_e32 v205, v74
	v_sub_f32_e32 v75, v77, v72
	v_add_f32_e32 v74, v202, v78
	v_exp_f32_e32 v206, v75
	v_sub_f32_e32 v75, v76, v72
	v_add_f32_e32 v74, v203, v74
	v_exp_f32_e32 v207, v75
	v_sub_f32_e32 v75, v137, v72
	v_add_f32_e32 v74, v204, v74
	v_exp_f32_e32 v137, v75
	v_sub_f32_e32 v70, v70, v72
	v_add_f32_e32 v74, v205, v74
	v_exp_f32_e32 v208, v70
	v_add_f32_e32 v70, v206, v74
	v_add_f32_e32 v70, v207, v70
	v_add_f32_e32 v70, v137, v70
	v_add_f32_e32 v70, v208, v70
	v_fmac_f32_e32 v70, v5, v4
	v_sub_f32_e32 v4, v136, v71
	v_exp_f32_e32 v5, v4
	v_sub_f32_e32 v4, v135, v71
	v_exp_f32_e32 v82, v4
	v_sub_f32_e32 v4, v99, v71
	v_exp_f32_e32 v83, v4
	v_sub_f32_e32 v4, v98, v71
	v_exp_f32_e32 v84, v4
	v_sub_f32_e32 v74, v101, v71
	v_add_f32_e32 v4, 0, v5
	v_exp_f32_e32 v85, v74
	v_sub_f32_e32 v74, v100, v71
	v_add_f32_e32 v4, v82, v4
	v_exp_f32_e32 v88, v74
	v_sub_f32_e32 v74, v95, v71
	v_add_f32_e32 v4, v83, v4
	v_exp_f32_e32 v89, v74
	v_sub_f32_e32 v74, v94, v71
	v_add_f32_e32 v4, v84, v4
	v_exp_f32_e32 v94, v74
	v_sub_f32_e32 v74, v97, v71
	v_add_f32_e32 v4, v85, v4
	v_exp_f32_e32 v95, v74
	v_sub_f32_e32 v74, v96, v71
	v_add_f32_e32 v4, v88, v4
	v_exp_f32_e32 v96, v74
	v_sub_f32_e32 v74, v91, v71
	v_add_f32_e32 v4, v89, v4
	v_exp_f32_e32 v97, v74
	v_sub_f32_e32 v74, v90, v71
	v_add_f32_e32 v4, v94, v4
	v_exp_f32_e32 v98, v74
	v_sub_f32_e32 v74, v93, v71
	v_add_f32_e32 v4, v95, v4
	v_exp_f32_e32 v99, v74
	v_sub_f32_e32 v74, v92, v71
	v_add_f32_e32 v4, v96, v4
	v_exp_f32_e32 v100, v74
	v_sub_f32_e32 v74, v87, v71
	v_add_f32_e32 v4, v97, v4
	v_exp_f32_e32 v101, v74
	v_sub_f32_e32 v74, v86, v71
	v_add_f32_e32 v4, v98, v4
	v_exp_f32_e32 v135, v74
	v_add_f32_e32 v4, v99, v4
	v_add_f32_e32 v4, v100, v4
	s_cmp_eq_u32 s83, 0
	v_add_f32_e32 v4, v101, v4
	s_cselect_b32 s0, 0x8000, s79
	v_add_f32_e32 v4, v135, v4
	s_add_i32 s0, s0, 0
	v_fmac_f32_e32 v4, v133, v2
	v_add_u32_e32 v2, s0, v142
	ds_read_b128 v[74:77], v2
	ds_read_b128 v[78:81], v2 offset:2048
	v_cvt_pk_bf16_f32 v83, v83, v84
	v_cvt_pk_bf16_f32 v84, v85, v88
	v_cvt_pk_bf16_f32 v85, v89, v94
	ds_read_b128 v[86:89], v2 offset:4096
	v_cvt_pk_bf16_f32 v82, v5, v82
	v_cvt_pk_bf16_f32 v90, v0, v73
	v_cvt_pk_bf16_f32 v91, v125, v134
	v_cvt_pk_bf16_f32 v92, v198, v199
	v_cvt_pk_bf16_f32 v93, v200, v201
	s_waitcnt lgkmcnt(2)
	v_mfma_f32_16x16x32_bf16 v[66:69], v[74:77], v[82:85], v[66:69]
	v_mfma_f32_16x16x32_bf16 v[34:37], v[74:77], v[90:93], v[34:37]
	ds_read_b128 v[74:77], v2 offset:6144
	s_waitcnt lgkmcnt(2)
	v_mfma_f32_16x16x32_bf16 v[62:65], v[78:81], v[82:85], v[62:65]
	v_mfma_f32_16x16x32_bf16 v[30:33], v[78:81], v[90:93], v[30:33]
	ds_read_b128 v[78:81], v2 offset:8192
	s_waitcnt lgkmcnt(2)
	v_mfma_f32_16x16x32_bf16 v[58:61], v[86:89], v[82:85], v[58:61]
	v_mfma_f32_16x16x32_bf16 v[26:29], v[86:89], v[90:93], v[26:29]
	ds_read_b128 v[86:89], v2 offset:10240
	s_waitcnt lgkmcnt(2)
	v_mfma_f32_16x16x32_bf16 v[54:57], v[74:77], v[82:85], v[54:57]
	v_mfma_f32_16x16x32_bf16 v[22:25], v[74:77], v[90:93], v[22:25]
	ds_read_b128 v[74:77], v2 offset:12288
	s_waitcnt lgkmcnt(2)
	v_mfma_f32_16x16x32_bf16 v[50:53], v[78:81], v[82:85], v[50:53]
	v_mfma_f32_16x16x32_bf16 v[18:21], v[78:81], v[90:93], v[18:21]
	ds_read_b128 v[78:81], v2 offset:14336
	v_add_u32_e32 v0, s0, v146
	s_waitcnt lgkmcnt(2)
	v_mfma_f32_16x16x32_bf16 v[46:49], v[86:89], v[82:85], v[46:49]
	v_mfma_f32_16x16x32_bf16 v[14:17], v[86:89], v[90:93], v[14:17]
	ds_read_b128 v[86:89], v0
	s_waitcnt lgkmcnt(2)
	v_mfma_f32_16x16x32_bf16 v[42:45], v[74:77], v[82:85], v[42:45]
	v_mfma_f32_16x16x32_bf16 v[10:13], v[74:77], v[90:93], v[10:13]
	ds_read_b128 v[74:77], v0 offset:2048
	s_waitcnt lgkmcnt(2)
	v_mfma_f32_16x16x32_bf16 v[38:41], v[78:81], v[82:85], v[38:41]
	v_cvt_pk_bf16_f32 v82, v202, v203
	v_cvt_pk_bf16_f32 v83, v204, v205
	v_cvt_pk_bf16_f32 v84, v206, v207
	v_mfma_f32_16x16x32_bf16 v[6:9], v[78:81], v[90:93], v[6:9]
	ds_read_b128 v[90:93], v0 offset:4096
	v_cvt_pk_bf16_f32 v78, v95, v96
	v_cvt_pk_bf16_f32 v79, v97, v98
	v_cvt_pk_bf16_f32 v80, v99, v100
	v_cvt_pk_bf16_f32 v81, v101, v135
	v_cvt_pk_bf16_f32 v85, v137, v208
	s_nop 0
	s_waitcnt lgkmcnt(2)
	v_mfma_f32_16x16x32_bf16 v[66:69], v[86:89], v[78:81], v[66:69]
	v_mfma_f32_16x16x32_bf16 v[34:37], v[86:89], v[82:85], v[34:37]
	ds_read_b128 v[86:89], v0 offset:6144
	s_waitcnt lgkmcnt(2)
	v_mfma_f32_16x16x32_bf16 v[62:65], v[74:77], v[78:81], v[62:65]
	v_mfma_f32_16x16x32_bf16 v[30:33], v[74:77], v[82:85], v[30:33]
	ds_read_b128 v[74:77], v0 offset:8192
	s_waitcnt lgkmcnt(2)
	v_mfma_f32_16x16x32_bf16 v[58:61], v[90:93], v[78:81], v[58:61]
	v_mfma_f32_16x16x32_bf16 v[26:29], v[90:93], v[82:85], v[26:29]
	ds_read_b128 v[90:93], v0 offset:10240
	s_waitcnt lgkmcnt(2)
	v_mfma_f32_16x16x32_bf16 v[54:57], v[86:89], v[78:81], v[54:57]
	v_mfma_f32_16x16x32_bf16 v[22:25], v[86:89], v[82:85], v[22:25]
	ds_read_b128 v[86:89], v0 offset:12288
	s_waitcnt lgkmcnt(2)
	v_mfma_f32_16x16x32_bf16 v[50:53], v[74:77], v[78:81], v[50:53]
	v_mfma_f32_16x16x32_bf16 v[18:21], v[74:77], v[82:85], v[18:21]
	ds_read_b128 v[74:77], v0 offset:14336
	s_waitcnt lgkmcnt(2)
	v_mfma_f32_16x16x32_bf16 v[46:49], v[90:93], v[78:81], v[46:49]
	v_mfma_f32_16x16x32_bf16 v[14:17], v[90:93], v[82:85], v[14:17]
	s_waitcnt lgkmcnt(1)
	v_mfma_f32_16x16x32_bf16 v[42:45], v[86:89], v[78:81], v[42:45]
	v_mfma_f32_16x16x32_bf16 v[10:13], v[86:89], v[82:85], v[10:13]
	s_waitcnt lgkmcnt(0)
	v_mfma_f32_16x16x32_bf16 v[38:41], v[74:77], v[78:81], v[38:41]
	s_waitcnt vmcnt(0)
	s_andn2_b64 vcc, exec, s[2:3]
	s_waitcnt vmcnt(0)
	v_mfma_f32_16x16x32_bf16 v[6:9], v[74:77], v[82:85], v[6:9]
	s_barrier
	s_cbranch_vccnz .LBB0_702
	s_branch .LBB0_782

.LBB0_789:
	s_lshl_b32 s2, s8, 1
	v_readlane_b32 s3, v253, 24
	s_add_u32 s8, s3, s2
	v_readlane_b32 s3, v253, 26
	s_addc_u32 s44, s3, 0
	v_readlane_b32 s3, v253, 28
	s_add_u32 s45, s3, s2
	v_readlane_b32 s2, v253, 30
	s_addc_u32 s46, s2, 0
	s_lshl_b32 s2, s22, 6
	s_lshl_b32 s22, s22, 13
	s_ashr_i32 s23, s22, 31
	s_lshl_b64 s[22:23], s[22:23], 1
	s_add_u32 s22, s8, s22
	s_addc_u32 s23, s44, s23
	s_ashr_i32 s3, s2, 31
	s_lshl_b64 s[2:3], s[2:3], 1
	s_mov_b32 m0, s28
	v_lshl_add_u64 v[4:5], s[22:23], 0, v[102:103]
	s_add_u32 s2, s45, s2
	global_load_lds_dwordx4 v[4:5], off
	v_lshl_add_u64 v[4:5], s[22:23], 0, v[108:109]
	s_mov_b32 m0, s81
	s_addc_u32 s3, s46, s3
	global_load_lds_dwordx4 v[4:5], off
	v_lshl_add_u64 v[4:5], s[2:3], 0, v[106:107]
	s_mov_b32 m0, s77
	s_andn2_b64 vcc, exec, s[0:1]
	global_load_lds_dwordx4 v[4:5], off
	v_lshl_add_u64 v[4:5], s[2:3], 0, v[112:113]
	s_mov_b32 m0, s78
	s_nop 0
	global_load_lds_dwordx4 v[4:5], off
	s_waitcnt vmcnt(0)
	s_waitcnt vmcnt(0) lgkmcnt(0)
	s_barrier
	s_cbranch_vccnz .LBB0_807
	v_readlane_b32 s0, v253, 38
	s_add_i32 s0, s0, s33
	v_mov_b32_e32 v4, v3
	v_mov_b32_e32 v5, v3
	s_sub_i32 s0, s0, s42
	v_mov_b32_e32 v2, v3
	v_mov_b64_e32 v[8:9], v[4:5]
	v_mov_b64_e32 v[12:13], v[4:5]
	v_mov_b64_e32 v[16:17], v[4:5]
	v_mov_b64_e32 v[20:21], v[4:5]
	v_mov_b64_e32 v[24:25], v[4:5]
	v_mov_b64_e32 v[28:29], v[4:5]
	v_mov_b64_e32 v[32:33], v[4:5]
	v_mov_b64_e32 v[36:37], v[4:5]
	v_mov_b64_e32 v[40:41], v[4:5]
	v_mov_b64_e32 v[44:45], v[4:5]
	v_mov_b64_e32 v[48:49], v[4:5]
	v_mov_b64_e32 v[52:53], v[4:5]
	v_mov_b64_e32 v[56:57], v[4:5]
	v_mov_b64_e32 v[60:61], v[4:5]
	v_mov_b64_e32 v[64:65], v[4:5]
	v_mov_b64_e32 v[68:69], v[4:5]
	s_sub_i32 s2, s0, s36
	s_mov_b32 s22, 0
	s_sub_i32 s3, 0, s42
	v_mov_b32_e32 v137, 0xf149f2ca
	v_mov_b32_e32 v136, 0
	v_mov_b32_e32 v135, 0
	v_mov_b64_e32 v[6:7], v[2:3]
	v_mov_b64_e32 v[10:11], v[2:3]
	v_mov_b64_e32 v[14:15], v[2:3]
	v_mov_b64_e32 v[18:19], v[2:3]
	v_mov_b64_e32 v[22:23], v[2:3]
	v_mov_b64_e32 v[26:27], v[2:3]
	v_mov_b64_e32 v[30:31], v[2:3]
	v_mov_b64_e32 v[34:35], v[2:3]
	v_mov_b64_e32 v[38:39], v[2:3]
	v_mov_b64_e32 v[42:43], v[2:3]
	v_mov_b64_e32 v[46:47], v[2:3]
	v_mov_b64_e32 v[50:51], v[2:3]
	v_mov_b64_e32 v[54:55], v[2:3]
	v_mov_b64_e32 v[58:59], v[2:3]
	v_mov_b64_e32 v[62:63], v[2:3]
	v_mov_b64_e32 v[66:67], v[2:3]
	v_mov_b32_e32 v4, 0xf149f2ca
	s_and_b32 s81, s22, 1
	s_add_i32 s47, s22, 1
	s_cmp_ge_i32 s22, s93
	s_cbranch_scc1 .LBB0_801
	s_branch .LBB0_792
	s_nop 0
	s_nop 0
	s_nop 0
	s_nop 0

.LBB0_801:
	s_lshl_b32 s0, s81, 14
	s_add_i32 s0, s0, 0
	v_add_u32_e32 v0, s0, v140
	ds_read_b128 v[70:73], v0
	ds_read_b128 v[74:77], v0 offset:4096
	ds_read_b128 v[78:81], v197
	ds_read_b128 v[82:85], v197 offset:4096
	ds_read_b128 v[86:89], v0 offset:8192
	ds_read_b128 v[94:97], v0 offset:12288
	s_waitcnt lgkmcnt(0)
	v_mfma_f32_16x16x32_bf16 v[90:93], v[70:73], v[78:81], 0
	v_mfma_f32_16x16x32_bf16 v[70:73], v[70:73], v[82:85], 0
	v_add_u32_e32 v0, s0, v143
	ds_read_b128 v[198:201], v0
	ds_read_b128 v[202:205], v197 offset:1024
	ds_read_b128 v[206:209], v197 offset:5120
	v_mfma_f32_16x16x32_bf16 v[98:101], v[74:77], v[78:81], 0
	v_mfma_f32_16x16x32_bf16 v[74:77], v[74:77], v[82:85], 0
	v_mfma_f32_16x16x32_bf16 v[210:213], v[86:89], v[78:81], 0
	ds_read_b128 v[214:217], v0 offset:4096
	v_mfma_f32_16x16x32_bf16 v[86:89], v[86:89], v[82:85], 0
	v_mfma_f32_16x16x32_bf16 v[78:81], v[94:97], v[78:81], 0
	v_mfma_f32_16x16x32_bf16 v[82:85], v[94:97], v[82:85], 0
	ds_read_b128 v[94:97], v0 offset:8192
	s_waitcnt lgkmcnt(3)
	v_mfma_f32_16x16x32_bf16 v[90:93], v[198:201], v[202:205], v[90:93]
	s_waitcnt lgkmcnt(2)
	v_mfma_f32_16x16x32_bf16 v[70:73], v[198:201], v[206:209], v[70:73]
	ds_read_b128 v[198:201], v0 offset:12288
	v_add_u32_e32 v0, s0, v144
	s_waitcnt lgkmcnt(2)
	v_mfma_f32_16x16x32_bf16 v[98:101], v[214:217], v[202:205], v[98:101]
	v_mfma_f32_16x16x32_bf16 v[74:77], v[214:217], v[206:209], v[74:77]
	ds_read_b128 v[214:217], v0
	ds_read_b128 v[218:221], v197 offset:2048
	ds_read_b128 v[222:225], v197 offset:6144
	s_waitcnt lgkmcnt(4)
	v_mfma_f32_16x16x32_bf16 v[210:213], v[94:97], v[202:205], v[210:213]
	v_mfma_f32_16x16x32_bf16 v[86:89], v[94:97], v[206:209], v[86:89]
	ds_read_b128 v[94:97], v0 offset:4096
	s_waitcnt lgkmcnt(4)
	v_mfma_f32_16x16x32_bf16 v[78:81], v[198:201], v[202:205], v[78:81]
	ds_read_b128 v[202:205], v0 offset:8192
	v_mfma_f32_16x16x32_bf16 v[82:85], v[198:201], v[206:209], v[82:85]
	s_waitcnt lgkmcnt(3)
	v_mfma_f32_16x16x32_bf16 v[90:93], v[214:217], v[218:221], v[90:93]
	ds_read_b128 v[198:201], v0 offset:12288
	s_waitcnt lgkmcnt(3)
	v_mfma_f32_16x16x32_bf16 v[70:73], v[214:217], v[222:225], v[70:73]
	v_add_u32_e32 v0, s0, v145
	s_waitcnt lgkmcnt(2)
	v_mfma_f32_16x16x32_bf16 v[206:209], v[94:97], v[218:221], v[98:101]
	v_mfma_f32_16x16x32_bf16 v[74:77], v[94:97], v[222:225], v[74:77]
	ds_read_b128 v[94:97], v0
	ds_read_b128 v[214:217], v197 offset:3072
	ds_read_b128 v[228:231], v197 offset:7168
	s_waitcnt lgkmcnt(4)
	v_mfma_f32_16x16x32_bf16 v[210:213], v[202:205], v[218:221], v[210:213]
	v_mfma_f32_16x16x32_bf16 v[86:89], v[202:205], v[222:225], v[86:89]
	ds_read_b128 v[202:205], v0 offset:4096
	ds_read_b128 v[232:235], v0 offset:8192
	s_waitcnt lgkmcnt(5)
	v_mfma_f32_16x16x32_bf16 v[218:221], v[198:201], v[218:221], v[78:81]
	v_mfma_f32_16x16x32_bf16 v[198:201], v[198:201], v[222:225], v[82:85]
	s_waitcnt lgkmcnt(3)
	v_mfma_f32_16x16x32_bf16 v[82:85], v[94:97], v[214:217], v[90:93]
	ds_read_b128 v[222:225], v0 offset:12288
	s_waitcnt lgkmcnt(3)
	v_mfma_f32_16x16x32_bf16 v[98:101], v[94:97], v[228:231], v[70:73]
	s_waitcnt lgkmcnt(2)
	v_mfma_f32_16x16x32_bf16 v[78:81], v[202:205], v[214:217], v[206:209]
	v_mfma_f32_16x16x32_bf16 v[94:97], v[202:205], v[228:231], v[74:77]
	s_waitcnt lgkmcnt(1)
	v_mfma_f32_16x16x32_bf16 v[74:77], v[232:235], v[214:217], v[210:213]
	v_mfma_f32_16x16x32_bf16 v[90:93], v[232:235], v[228:231], v[86:89]
	s_nop 0
	v_max_f32_e32 v0, v82, v83
	s_waitcnt lgkmcnt(0)
	v_mfma_f32_16x16x32_bf16 v[70:73], v[222:225], v[214:217], v[218:221]
	v_max_f32_e32 v2, v84, v85
	s_nop 0
	v_max_f32_e32 v5, v80, v81
	v_max3_f32 v5, v78, v79, v5
	v_max3_f32 v0, v0, v2, v5
	v_max_f32_e32 v2, v76, v77
	s_nop 1
	v_max_f32_e32 v5, v72, v73
	v_max3_f32 v2, v74, v75, v2
	v_max3_f32 v5, v70, v71, v5
	v_max3_f32 v0, v0, v2, v5
	v_mov_b32_e32 v2, v0
	s_nop 1
	v_permlane16_swap_b32_e32 v0, v2
	ds_read_b32 v125, v196 offset:508
	v_max_f32_e32 v0, v0, v2
	v_mov_b32_e32 v2, v0
	s_nop 1
	v_permlane32_swap_b32_e32 v0, v2
	v_max_f32_e32 v0, v0, v2
	s_waitcnt lgkmcnt(0)
	v_fmamk_f32 v0, v0, 0x3fb8aa3b, v125
	v_max_f32_e32 v133, v137, v0
	v_sub_f32_e32 v0, v137, v133
	v_exp_f32_e32 v2, v0
	v_mfma_f32_16x16x32_bf16 v[86:89], v[222:225], v[228:231], v[198:201]
	v_cmp_neq_f32_e32 vcc, 1.0, v2
	s_cbranch_vccz .LBB0_803
	v_pk_mul_f32 v[68:69], v[68:69], v[2:3] op_sel_hi:[1,0]
	v_pk_mul_f32 v[66:67], v[66:67], v[2:3] op_sel_hi:[1,0]
	v_pk_mul_f32 v[64:65], v[64:65], v[2:3] op_sel_hi:[1,0]
	v_pk_mul_f32 v[62:63], v[62:63], v[2:3] op_sel_hi:[1,0]
	v_pk_mul_f32 v[60:61], v[60:61], v[2:3] op_sel_hi:[1,0]
	v_pk_mul_f32 v[58:59], v[58:59], v[2:3] op_sel_hi:[1,0]
	v_pk_mul_f32 v[56:57], v[56:57], v[2:3] op_sel_hi:[1,0]
	v_pk_mul_f32 v[54:55], v[54:55], v[2:3] op_sel_hi:[1,0]
	v_pk_mul_f32 v[52:53], v[52:53], v[2:3] op_sel_hi:[1,0]
	v_pk_mul_f32 v[50:51], v[50:51], v[2:3] op_sel_hi:[1,0]
	v_pk_mul_f32 v[48:49], v[48:49], v[2:3] op_sel_hi:[1,0]
	v_pk_mul_f32 v[46:47], v[46:47], v[2:3] op_sel_hi:[1,0]
	v_pk_mul_f32 v[44:45], v[44:45], v[2:3] op_sel_hi:[1,0]
	v_pk_mul_f32 v[42:43], v[42:43], v[2:3] op_sel_hi:[1,0]
	v_pk_mul_f32 v[40:41], v[40:41], v[2:3] op_sel_hi:[1,0]
	v_pk_mul_f32 v[38:39], v[38:39], v[2:3] op_sel_hi:[1,0]
.LBB0_803:
	v_max_f32_e32 v0, v98, v99
	v_max_f32_e32 v5, v100, v101
	v_max_f32_e32 v134, v96, v97
	v_max3_f32 v134, v94, v95, v134
	v_max3_f32 v0, v0, v5, v134
	v_max_f32_e32 v5, v92, v93
	v_max_f32_e32 v134, v88, v89
	v_max3_f32 v5, v90, v91, v5
	v_max3_f32 v134, v86, v87, v134
	v_max3_f32 v0, v0, v5, v134
	v_mov_b32_e32 v5, v0
	s_nop 1
	v_permlane16_swap_b32_e32 v0, v5
	v_max_f32_e32 v0, v0, v5
	v_mov_b32_e32 v5, v0
	s_nop 1
	v_permlane32_swap_b32_e32 v0, v5
	v_max_f32_e32 v0, v0, v5
	v_fmamk_f32 v0, v0, 0x3fb8aa3b, v125
	v_max_f32_e32 v5, v4, v4
	v_max_f32_e32 v134, v5, v0
	v_sub_f32_e32 v0, v4, v134
	v_exp_f32_e32 v4, v0
	s_nop 0
	v_cmp_neq_f32_e32 vcc, 1.0, v4
	s_cbranch_vccz .LBB0_805
	v_pk_mul_f32 v[36:37], v[36:37], v[4:5] op_sel_hi:[1,0]
	v_pk_mul_f32 v[34:35], v[34:35], v[4:5] op_sel_hi:[1,0]
	v_pk_mul_f32 v[32:33], v[32:33], v[4:5] op_sel_hi:[1,0]
	v_pk_mul_f32 v[30:31], v[30:31], v[4:5] op_sel_hi:[1,0]
	v_pk_mul_f32 v[28:29], v[28:29], v[4:5] op_sel_hi:[1,0]
	v_pk_mul_f32 v[26:27], v[26:27], v[4:5] op_sel_hi:[1,0]
	v_pk_mul_f32 v[24:25], v[24:25], v[4:5] op_sel_hi:[1,0]
	v_pk_mul_f32 v[22:23], v[22:23], v[4:5] op_sel_hi:[1,0]
	v_pk_mul_f32 v[20:21], v[20:21], v[4:5] op_sel_hi:[1,0]
	v_pk_mul_f32 v[18:19], v[18:19], v[4:5] op_sel_hi:[1,0]
	v_pk_mul_f32 v[16:17], v[16:17], v[4:5] op_sel_hi:[1,0]
	v_pk_mul_f32 v[14:15], v[14:15], v[4:5] op_sel_hi:[1,0]
	v_pk_mul_f32 v[12:13], v[12:13], v[4:5] op_sel_hi:[1,0]
	v_pk_mul_f32 v[10:11], v[10:11], v[4:5] op_sel_hi:[1,0]
	v_pk_mul_f32 v[8:9], v[8:9], v[4:5] op_sel_hi:[1,0]
	v_pk_mul_f32 v[6:7], v[6:7], v[4:5] op_sel_hi:[1,0]
.LBB0_805:
	v_sub_f32_e32 v0, v125, v134
	v_fmamk_f32 v5, v98, 0x3fb8aa3b, v0
	v_exp_f32_e32 v98, v5
	v_fmamk_f32 v5, v99, 0x3fb8aa3b, v0
	v_exp_f32_e32 v99, v5
	v_fmamk_f32 v5, v100, 0x3fb8aa3b, v0
	v_exp_f32_e32 v100, v5
	v_fmamk_f32 v5, v101, 0x3fb8aa3b, v0
	v_exp_f32_e32 v101, v5
	v_fmamk_f32 v94, v94, 0x3fb8aa3b, v0
	v_add_f32_e32 v5, 0, v98
	v_exp_f32_e32 v94, v94
	v_fmamk_f32 v95, v95, 0x3fb8aa3b, v0
	v_add_f32_e32 v5, v99, v5
	v_exp_f32_e32 v95, v95
	v_fmamk_f32 v96, v96, 0x3fb8aa3b, v0
	v_add_f32_e32 v5, v100, v5
	v_exp_f32_e32 v96, v96
	v_fmamk_f32 v97, v97, 0x3fb8aa3b, v0
	v_add_f32_e32 v5, v101, v5
	v_exp_f32_e32 v97, v97
	v_fmamk_f32 v90, v90, 0x3fb8aa3b, v0
	v_add_f32_e32 v5, v94, v5
	v_exp_f32_e32 v90, v90
	v_fmamk_f32 v91, v91, 0x3fb8aa3b, v0
	v_add_f32_e32 v5, v95, v5
	v_exp_f32_e32 v91, v91
	v_fmamk_f32 v92, v92, 0x3fb8aa3b, v0
	v_add_f32_e32 v5, v96, v5
	v_exp_f32_e32 v92, v92
	v_fmamk_f32 v93, v93, 0x3fb8aa3b, v0
	v_add_f32_e32 v5, v97, v5
	v_exp_f32_e32 v93, v93
	v_fmamk_f32 v86, v86, 0x3fb8aa3b, v0
	v_add_f32_e32 v5, v90, v5
	v_exp_f32_e32 v137, v86
	v_fmamk_f32 v86, v87, 0x3fb8aa3b, v0
	v_add_f32_e32 v5, v91, v5
	v_exp_f32_e32 v198, v86
	v_fmamk_f32 v86, v88, 0x3fb8aa3b, v0
	v_add_f32_e32 v5, v92, v5
	v_exp_f32_e32 v199, v86
	v_fmac_f32_e32 v0, 0x3fb8aa3b, v89
	v_add_f32_e32 v5, v93, v5
	v_exp_f32_e32 v0, v0
	v_add_f32_e32 v5, v137, v5
	v_add_f32_e32 v5, v198, v5
	v_add_f32_e32 v5, v199, v5
	v_add_f32_e32 v5, v0, v5
	v_fmac_f32_e32 v5, v136, v4
	v_sub_f32_e32 v4, v125, v133
	v_fmamk_f32 v82, v82, 0x3fb8aa3b, v4
	v_exp_f32_e32 v82, v82
	v_fmamk_f32 v83, v83, 0x3fb8aa3b, v4
	v_exp_f32_e32 v83, v83
	v_fmamk_f32 v84, v84, 0x3fb8aa3b, v4
	v_exp_f32_e32 v84, v84
	v_fmamk_f32 v85, v85, 0x3fb8aa3b, v4
	v_exp_f32_e32 v85, v85
	v_fmamk_f32 v78, v78, 0x3fb8aa3b, v4
	v_add_f32_e32 v86, 0, v82
	v_exp_f32_e32 v87, v78
	v_fmamk_f32 v78, v79, 0x3fb8aa3b, v4
	v_add_f32_e32 v86, v83, v86
	v_exp_f32_e32 v88, v78
	v_fmamk_f32 v78, v80, 0x3fb8aa3b, v4
	v_add_f32_e32 v86, v84, v86
	v_exp_f32_e32 v89, v78
	v_fmamk_f32 v78, v81, 0x3fb8aa3b, v4
	v_add_f32_e32 v86, v85, v86
	v_exp_f32_e32 v81, v78
	v_fmamk_f32 v74, v74, 0x3fb8aa3b, v4
	v_add_f32_e32 v78, v87, v86
	v_exp_f32_e32 v136, v74
	v_fmamk_f32 v74, v75, 0x3fb8aa3b, v4
	v_add_f32_e32 v78, v88, v78
	v_exp_f32_e32 v200, v74
	v_fmamk_f32 v74, v76, 0x3fb8aa3b, v4
	v_add_f32_e32 v78, v89, v78
	v_exp_f32_e32 v201, v74
	v_fmamk_f32 v74, v77, 0x3fb8aa3b, v4
	v_add_f32_e32 v78, v81, v78
	v_exp_f32_e32 v202, v74
	v_fmamk_f32 v70, v70, 0x3fb8aa3b, v4
	v_add_f32_e32 v74, v136, v78
	v_exp_f32_e32 v203, v70
	v_fmamk_f32 v70, v71, 0x3fb8aa3b, v4
	v_add_f32_e32 v74, v200, v74
	v_exp_f32_e32 v204, v70
	v_fmamk_f32 v70, v72, 0x3fb8aa3b, v4
	v_add_f32_e32 v74, v201, v74
	v_exp_f32_e32 v205, v70
	v_fmac_f32_e32 v4, 0x3fb8aa3b, v73
	v_add_f32_e32 v74, v202, v74
	v_exp_f32_e32 v4, v4
	v_add_f32_e32 v70, v203, v74
	s_cmp_eq_u32 s81, 0
	v_add_f32_e32 v70, v204, v70
	v_add_f32_e32 v70, v205, v70
	s_cselect_b32 s0, 0x8000, s79
	v_add_f32_e32 v125, v4, v70
	s_add_i32 s0, s0, 0
	v_fmac_f32_e32 v125, v135, v2
	v_add_u32_e32 v2, s0, v142
	ds_read_b128 v[70:73], v2
	ds_read_b128 v[74:77], v2 offset:2048
	v_cvt_pk_bf16_f32 v78, v82, v83
	v_cvt_pk_bf16_f32 v79, v84, v85
	ds_read_b128 v[82:85], v2 offset:4096
	v_cvt_pk_bf16_f32 v80, v87, v88
	v_cvt_pk_bf16_f32 v81, v89, v81
	v_cvt_pk_bf16_f32 v86, v98, v99
	v_cvt_pk_bf16_f32 v87, v100, v101
	v_cvt_pk_bf16_f32 v88, v94, v95
	v_cvt_pk_bf16_f32 v89, v96, v97
	s_waitcnt lgkmcnt(2)
	v_mfma_f32_16x16x32_bf16 v[66:69], v[70:73], v[78:81], v[66:69]
	v_mfma_f32_16x16x32_bf16 v[34:37], v[70:73], v[86:89], v[34:37]
	ds_read_b128 v[70:73], v2 offset:6144
	s_waitcnt lgkmcnt(2)
	v_mfma_f32_16x16x32_bf16 v[62:65], v[74:77], v[78:81], v[62:65]
	v_mfma_f32_16x16x32_bf16 v[30:33], v[74:77], v[86:89], v[30:33]
	ds_read_b128 v[74:77], v2 offset:8192
	s_waitcnt lgkmcnt(2)
	v_mfma_f32_16x16x32_bf16 v[58:61], v[82:85], v[78:81], v[58:61]
	v_mfma_f32_16x16x32_bf16 v[26:29], v[82:85], v[86:89], v[26:29]
	ds_read_b128 v[82:85], v2 offset:10240
	s_waitcnt lgkmcnt(2)
	v_mfma_f32_16x16x32_bf16 v[54:57], v[70:73], v[78:81], v[54:57]
	v_mfma_f32_16x16x32_bf16 v[22:25], v[70:73], v[86:89], v[22:25]
	ds_read_b128 v[70:73], v2 offset:12288
	s_waitcnt lgkmcnt(2)
	v_mfma_f32_16x16x32_bf16 v[50:53], v[74:77], v[78:81], v[50:53]
	v_mfma_f32_16x16x32_bf16 v[18:21], v[74:77], v[86:89], v[18:21]
	ds_read_b128 v[74:77], v2 offset:14336
	v_add_u32_e32 v2, s0, v146
	s_waitcnt lgkmcnt(2)
	v_mfma_f32_16x16x32_bf16 v[46:49], v[82:85], v[78:81], v[46:49]
	v_mfma_f32_16x16x32_bf16 v[14:17], v[82:85], v[86:89], v[14:17]
	ds_read_b128 v[82:85], v2
	s_waitcnt lgkmcnt(2)
	v_mfma_f32_16x16x32_bf16 v[42:45], v[70:73], v[78:81], v[42:45]
	v_mfma_f32_16x16x32_bf16 v[10:13], v[70:73], v[86:89], v[10:13]
	ds_read_b128 v[70:73], v2 offset:2048
	s_waitcnt lgkmcnt(2)
	v_mfma_f32_16x16x32_bf16 v[38:41], v[74:77], v[78:81], v[38:41]
	v_cvt_pk_bf16_f32 v78, v90, v91
	v_cvt_pk_bf16_f32 v79, v92, v93
	v_cvt_pk_bf16_f32 v80, v137, v198
	v_mfma_f32_16x16x32_bf16 v[6:9], v[74:77], v[86:89], v[6:9]
	ds_read_b128 v[86:89], v2 offset:4096
	v_cvt_pk_bf16_f32 v74, v136, v200
	v_cvt_pk_bf16_f32 v75, v201, v202
	v_cvt_pk_bf16_f32 v76, v203, v204
	v_cvt_pk_bf16_f32 v77, v205, v4
	v_cvt_pk_bf16_f32 v81, v199, v0
	s_nop 0
	s_waitcnt lgkmcnt(2)
	v_mfma_f32_16x16x32_bf16 v[66:69], v[82:85], v[74:77], v[66:69]
	v_mfma_f32_16x16x32_bf16 v[34:37], v[82:85], v[78:81], v[34:37]
	ds_read_b128 v[82:85], v2 offset:6144
	s_waitcnt lgkmcnt(2)
	v_mfma_f32_16x16x32_bf16 v[62:65], v[70:73], v[74:77], v[62:65]
	v_mfma_f32_16x16x32_bf16 v[30:33], v[70:73], v[78:81], v[30:33]
	ds_read_b128 v[70:73], v2 offset:8192
	s_waitcnt lgkmcnt(2)
	v_mfma_f32_16x16x32_bf16 v[58:61], v[86:89], v[74:77], v[58:61]
	v_mfma_f32_16x16x32_bf16 v[26:29], v[86:89], v[78:81], v[26:29]
	ds_read_b128 v[86:89], v2 offset:10240
	s_waitcnt lgkmcnt(2)
	v_mfma_f32_16x16x32_bf16 v[54:57], v[82:85], v[74:77], v[54:57]
	v_mfma_f32_16x16x32_bf16 v[22:25], v[82:85], v[78:81], v[22:25]
	ds_read_b128 v[82:85], v2 offset:12288
	s_waitcnt lgkmcnt(2)
	v_mfma_f32_16x16x32_bf16 v[50:53], v[70:73], v[74:77], v[50:53]
	v_mfma_f32_16x16x32_bf16 v[18:21], v[70:73], v[78:81], v[18:21]
	ds_read_b128 v[70:73], v2 offset:14336
	s_waitcnt lgkmcnt(2)
	v_mfma_f32_16x16x32_bf16 v[46:49], v[86:89], v[74:77], v[46:49]
	v_mfma_f32_16x16x32_bf16 v[14:17], v[86:89], v[78:81], v[14:17]
	s_waitcnt lgkmcnt(1)
	v_mfma_f32_16x16x32_bf16 v[42:45], v[82:85], v[74:77], v[42:45]
	v_mfma_f32_16x16x32_bf16 v[10:13], v[82:85], v[78:81], v[10:13]
	s_waitcnt lgkmcnt(0)
	v_mfma_f32_16x16x32_bf16 v[38:41], v[70:73], v[74:77], v[38:41]
	s_waitcnt vmcnt(0)
	s_add_i32 s0, s3, s47
	s_cmp_lg_u32 s0, 0
	v_mfma_f32_16x16x32_bf16 v[6:9], v[70:73], v[78:81], v[6:9]
	s_waitcnt vmcnt(0)
	s_barrier
	s_cbranch_scc1 .LBB0_791
	s_cmp_gt_i32 s37, s93
	s_cbranch_scc1 .LBB0_517
	s_branch .LBB0_808

.LBB0_808:
	s_sub_i32 s0, s33, s42
	s_sub_i32 s47, s0, s43
	s_add_i32 s23, s37, -1
	s_sub_i32 s81, 0, s42
	s_add_i32 s82, s23, 1
	s_cmp_lt_i32 s82, s42
	s_mov_b64 s[0:1], -1
	s_cbranch_scc1 .LBB0_815
	s_branch .LBB0_810
	s_nop 0
	s_nop 0
	s_nop 0
	s_nop 0
	s_nop 0
	s_nop 0

.LBB0_827:
	s_lshl_b32 s2, s83, 14
	s_add_i32 s2, s2, 0
	v_add_u32_e32 v0, s2, v140
	ds_read_b128 v[70:73], v0
	ds_read_b128 v[74:77], v0 offset:4096
	ds_read_b128 v[78:81], v197
	ds_read_b128 v[82:85], v197 offset:4096
	ds_read_b128 v[86:89], v0 offset:8192
	ds_read_b128 v[94:97], v0 offset:12288
	s_waitcnt lgkmcnt(0)
	v_mfma_f32_16x16x32_bf16 v[90:93], v[70:73], v[78:81], 0
	v_mfma_f32_16x16x32_bf16 v[70:73], v[70:73], v[82:85], 0
	v_add_u32_e32 v0, s2, v143
	ds_read_b128 v[198:201], v0
	ds_read_b128 v[202:205], v197 offset:1024
	ds_read_b128 v[206:209], v197 offset:5120
	v_mfma_f32_16x16x32_bf16 v[98:101], v[74:77], v[78:81], 0
	v_mfma_f32_16x16x32_bf16 v[74:77], v[74:77], v[82:85], 0
	v_mfma_f32_16x16x32_bf16 v[210:213], v[86:89], v[78:81], 0
	ds_read_b128 v[214:217], v0 offset:4096
	v_mfma_f32_16x16x32_bf16 v[86:89], v[86:89], v[82:85], 0
	v_mfma_f32_16x16x32_bf16 v[78:81], v[94:97], v[78:81], 0
	v_mfma_f32_16x16x32_bf16 v[82:85], v[94:97], v[82:85], 0
	ds_read_b128 v[94:97], v0 offset:8192
	s_waitcnt lgkmcnt(3)
	v_mfma_f32_16x16x32_bf16 v[90:93], v[198:201], v[202:205], v[90:93]
	s_waitcnt lgkmcnt(2)
	v_mfma_f32_16x16x32_bf16 v[70:73], v[198:201], v[206:209], v[70:73]
	ds_read_b128 v[198:201], v0 offset:12288
	v_add_u32_e32 v0, s2, v144
	s_waitcnt lgkmcnt(2)
	v_mfma_f32_16x16x32_bf16 v[98:101], v[214:217], v[202:205], v[98:101]
	v_mfma_f32_16x16x32_bf16 v[74:77], v[214:217], v[206:209], v[74:77]
	ds_read_b128 v[214:217], v0
	ds_read_b128 v[218:221], v197 offset:2048
	ds_read_b128 v[222:225], v197 offset:6144
	s_waitcnt lgkmcnt(4)
	v_mfma_f32_16x16x32_bf16 v[210:213], v[94:97], v[202:205], v[210:213]
	v_mfma_f32_16x16x32_bf16 v[86:89], v[94:97], v[206:209], v[86:89]
	ds_read_b128 v[94:97], v0 offset:4096
	s_waitcnt lgkmcnt(4)
	v_mfma_f32_16x16x32_bf16 v[78:81], v[198:201], v[202:205], v[78:81]
	ds_read_b128 v[202:205], v0 offset:8192
	v_mfma_f32_16x16x32_bf16 v[82:85], v[198:201], v[206:209], v[82:85]
	s_waitcnt lgkmcnt(3)
	v_mfma_f32_16x16x32_bf16 v[90:93], v[214:217], v[218:221], v[90:93]
	ds_read_b128 v[198:201], v0 offset:12288
	s_waitcnt lgkmcnt(3)
	v_mfma_f32_16x16x32_bf16 v[70:73], v[214:217], v[222:225], v[70:73]
	v_add_u32_e32 v0, s2, v145
	s_waitcnt lgkmcnt(2)
	v_mfma_f32_16x16x32_bf16 v[206:209], v[94:97], v[218:221], v[98:101]
	v_mfma_f32_16x16x32_bf16 v[74:77], v[94:97], v[222:225], v[74:77]
	ds_read_b128 v[94:97], v0
	ds_read_b128 v[214:217], v197 offset:3072
	ds_read_b128 v[228:231], v197 offset:7168
	s_waitcnt lgkmcnt(4)
	v_mfma_f32_16x16x32_bf16 v[210:213], v[202:205], v[218:221], v[210:213]
	v_mfma_f32_16x16x32_bf16 v[86:89], v[202:205], v[222:225], v[86:89]
	ds_read_b128 v[202:205], v0 offset:4096
	ds_read_b128 v[232:235], v0 offset:8192
	s_waitcnt lgkmcnt(5)
	v_mfma_f32_16x16x32_bf16 v[218:221], v[198:201], v[218:221], v[78:81]
	v_mfma_f32_16x16x32_bf16 v[198:201], v[198:201], v[222:225], v[82:85]
	s_waitcnt lgkmcnt(2)
	v_mfma_f32_16x16x32_bf16 v[82:85], v[94:97], v[228:231], v[70:73]
	s_nop 2
	ds_read_b128 v[70:73], v0 offset:12288
	v_mfma_f32_16x16x32_bf16 v[98:101], v[94:97], v[214:217], v[90:93]
	s_waitcnt lgkmcnt(2)
	v_mfma_f32_16x16x32_bf16 v[94:97], v[202:205], v[214:217], v[206:209]
	v_mfma_f32_16x16x32_bf16 v[78:81], v[202:205], v[228:231], v[74:77]
	s_waitcnt lgkmcnt(1)
	v_mfma_f32_16x16x32_bf16 v[90:93], v[232:235], v[214:217], v[210:213]
	v_mfma_f32_16x16x32_bf16 v[74:77], v[232:235], v[228:231], v[86:89]
	s_waitcnt lgkmcnt(0)
	v_mfma_f32_16x16x32_bf16 v[86:89], v[70:73], v[214:217], v[218:221]
	s_lshl_b32 s33, s22, 6
	v_subrev_u32_e32 v2, s33, v189
	v_cmp_gt_u32_e32 vcc, s80, v2
	v_mfma_f32_16x16x32_bf16 v[70:73], v[70:73], v[228:231], v[198:201]
	v_mov_b32_e32 v135, 0xff800000
	v_mov_b32_e32 v136, 0xff800000
	s_and_saveexec_b64 s[2:3], vcc
	s_cbranch_execz .LBB0_829
	v_min_u32_e32 v0, 0x7f, v2
	v_lshl_add_u32 v0, v0, 2, v196
	ds_read_b32 v136, v0
	s_waitcnt lgkmcnt(0)
	v_fmac_f32_e32 v136, 0x3fb8aa3b, v98

.LBB0_891:
	s_or_b64 exec, exec, s[2:3]
	v_max_f32_e32 v0, v136, v135
	v_max3_f32 v0, v0, v99, v98
	v_max3_f32 v0, v0, v101, v100
	v_max3_f32 v0, v0, v95, v94
	v_max3_f32 v0, v0, v97, v96
	v_max3_f32 v0, v0, v91, v90
	v_max3_f32 v0, v0, v93, v92
	v_max3_f32 v0, v0, v87, v86
	v_mov_b32_e32 v2, v0
	s_nop 1
	v_permlane16_swap_b32_e32 v0, v2
	v_max_f32_e32 v0, v0, v2
	v_mov_b32_e32 v2, v0
	s_nop 1
	v_permlane32_swap_b32_e32 v0, v2
	v_max3_f32 v71, v133, v0, v2
	v_sub_f32_e32 v0, v133, v71
	v_exp_f32_e32 v2, v0
	s_nop 0
	v_cmp_neq_f32_e32 vcc, 1.0, v2
	s_cbranch_vccz .LBB0_893
	v_pk_mul_f32 v[68:69], v[68:69], v[2:3] op_sel_hi:[1,0]
	v_pk_mul_f32 v[66:67], v[66:67], v[2:3] op_sel_hi:[1,0]
	v_pk_mul_f32 v[64:65], v[64:65], v[2:3] op_sel_hi:[1,0]
	v_pk_mul_f32 v[62:63], v[62:63], v[2:3] op_sel_hi:[1,0]
	v_pk_mul_f32 v[60:61], v[60:61], v[2:3] op_sel_hi:[1,0]
	v_pk_mul_f32 v[58:59], v[58:59], v[2:3] op_sel_hi:[1,0]
	v_pk_mul_f32 v[56:57], v[56:57], v[2:3] op_sel_hi:[1,0]
	v_pk_mul_f32 v[54:55], v[54:55], v[2:3] op_sel_hi:[1,0]
	v_pk_mul_f32 v[52:53], v[52:53], v[2:3] op_sel_hi:[1,0]
	v_pk_mul_f32 v[50:51], v[50:51], v[2:3] op_sel_hi:[1,0]
	v_pk_mul_f32 v[48:49], v[48:49], v[2:3] op_sel_hi:[1,0]
	v_pk_mul_f32 v[46:47], v[46:47], v[2:3] op_sel_hi:[1,0]
	v_pk_mul_f32 v[44:45], v[44:45], v[2:3] op_sel_hi:[1,0]
	v_pk_mul_f32 v[42:43], v[42:43], v[2:3] op_sel_hi:[1,0]
	v_pk_mul_f32 v[40:41], v[40:41], v[2:3] op_sel_hi:[1,0]
	v_pk_mul_f32 v[38:39], v[38:39], v[2:3] op_sel_hi:[1,0]

.LBB0_895:
	v_sub_f32_e32 v0, v89, v72
	v_exp_f32_e32 v0, v0
	v_sub_f32_e32 v73, v88, v72
	v_exp_f32_e32 v73, v73
	v_sub_f32_e32 v83, v83, v72
	v_exp_f32_e32 v133, v83
	v_sub_f32_e32 v82, v82, v72
	v_exp_f32_e32 v134, v82
	v_sub_f32_e32 v83, v85, v72
	v_add_f32_e32 v82, 0, v0
	v_exp_f32_e32 v198, v83
	v_sub_f32_e32 v83, v84, v72
	v_add_f32_e32 v82, v73, v82
	v_exp_f32_e32 v199, v83
	v_sub_f32_e32 v79, v79, v72
	v_add_f32_e32 v82, v133, v82
	v_exp_f32_e32 v200, v79
	v_sub_f32_e32 v78, v78, v72
	v_add_f32_e32 v82, v134, v82
	v_exp_f32_e32 v201, v78
	v_sub_f32_e32 v79, v81, v72
	v_add_f32_e32 v78, v198, v82
	v_exp_f32_e32 v202, v79
	v_sub_f32_e32 v79, v80, v72
	v_add_f32_e32 v78, v199, v78
	v_exp_f32_e32 v203, v79
	v_sub_f32_e32 v75, v75, v72
	v_add_f32_e32 v78, v200, v78
	v_exp_f32_e32 v204, v75
	v_sub_f32_e32 v74, v74, v72
	v_add_f32_e32 v78, v201, v78
	v_exp_f32_e32 v205, v74
	v_sub_f32_e32 v75, v77, v72
	v_add_f32_e32 v74, v202, v78
	v_exp_f32_e32 v206, v75
	v_sub_f32_e32 v75, v76, v72
	v_add_f32_e32 v74, v203, v74
	v_exp_f32_e32 v207, v75
	v_sub_f32_e32 v75, v137, v72
	v_add_f32_e32 v74, v204, v74
	v_exp_f32_e32 v137, v75
	v_sub_f32_e32 v70, v70, v72
	v_add_f32_e32 v74, v205, v74
	v_exp_f32_e32 v208, v70
	v_add_f32_e32 v70, v206, v74
	v_add_f32_e32 v70, v207, v70
	v_add_f32_e32 v70, v137, v70
	v_add_f32_e32 v70, v208, v70
	v_fmac_f32_e32 v70, v5, v4
	v_sub_f32_e32 v4, v136, v71
	v_exp_f32_e32 v5, v4
	v_sub_f32_e32 v4, v135, v71
	v_exp_f32_e32 v82, v4
	v_sub_f32_e32 v4, v99, v71
	v_exp_f32_e32 v83, v4
	v_sub_f32_e32 v4, v98, v71
	v_exp_f32_e32 v84, v4
	v_sub_f32_e32 v74, v101, v71
	v_add_f32_e32 v4, 0, v5
	v_exp_f32_e32 v85, v74
	v_sub_f32_e32 v74, v100, v71
	v_add_f32_e32 v4, v82, v4
	v_exp_f32_e32 v88, v74
	v_sub_f32_e32 v74, v95, v71
	v_add_f32_e32 v4, v83, v4
	v_exp_f32_e32 v89, v74
	v_sub_f32_e32 v74, v94, v71
	v_add_f32_e32 v4, v84, v4
	v_exp_f32_e32 v94, v74
	v_sub_f32_e32 v74, v97, v71
	v_add_f32_e32 v4, v85, v4
	v_exp_f32_e32 v95, v74
	v_sub_f32_e32 v74, v96, v71
	v_add_f32_e32 v4, v88, v4
	v_exp_f32_e32 v96, v74
	v_sub_f32_e32 v74, v91, v71
	v_add_f32_e32 v4, v89, v4
	v_exp_f32_e32 v97, v74
	v_sub_f32_e32 v74, v90, v71
	v_add_f32_e32 v4, v94, v4
	v_exp_f32_e32 v98, v74
	v_sub_f32_e32 v74, v93, v71
	v_add_f32_e32 v4, v95, v4
	v_exp_f32_e32 v99, v74
	v_sub_f32_e32 v74, v92, v71
	v_add_f32_e32 v4, v96, v4
	v_exp_f32_e32 v100, v74
	v_sub_f32_e32 v74, v87, v71
	v_add_f32_e32 v4, v97, v4
	v_exp_f32_e32 v101, v74
	v_sub_f32_e32 v74, v86, v71
	v_add_f32_e32 v4, v98, v4
	v_exp_f32_e32 v135, v74
	v_add_f32_e32 v4, v99, v4
	v_add_f32_e32 v4, v100, v4
	s_cmp_eq_u32 s83, 0
	v_add_f32_e32 v4, v101, v4
	s_cselect_b32 s2, 0x8000, s79
	v_add_f32_e32 v4, v135, v4
	s_add_i32 s2, s2, 0
	v_fmac_f32_e32 v4, v125, v2
	v_add_u32_e32 v2, s2, v142
	ds_read_b128 v[74:77], v2
	ds_read_b128 v[78:81], v2 offset:2048
	v_cvt_pk_bf16_f32 v83, v83, v84
	v_cvt_pk_bf16_f32 v84, v85, v88
	v_cvt_pk_bf16_f32 v85, v89, v94
	ds_read_b128 v[86:89], v2 offset:4096
	v_cvt_pk_bf16_f32 v82, v5, v82
	v_cvt_pk_bf16_f32 v90, v0, v73
	v_cvt_pk_bf16_f32 v91, v133, v134
	v_cvt_pk_bf16_f32 v92, v198, v199
	v_cvt_pk_bf16_f32 v93, v200, v201
	s_waitcnt lgkmcnt(2)
	v_mfma_f32_16x16x32_bf16 v[66:69], v[74:77], v[82:85], v[66:69]
	v_mfma_f32_16x16x32_bf16 v[34:37], v[74:77], v[90:93], v[34:37]
	ds_read_b128 v[74:77], v2 offset:6144
	s_waitcnt lgkmcnt(2)
	v_mfma_f32_16x16x32_bf16 v[62:65], v[78:81], v[82:85], v[62:65]
	v_mfma_f32_16x16x32_bf16 v[30:33], v[78:81], v[90:93], v[30:33]
	ds_read_b128 v[78:81], v2 offset:8192
	s_waitcnt lgkmcnt(2)
	v_mfma_f32_16x16x32_bf16 v[58:61], v[86:89], v[82:85], v[58:61]
	v_mfma_f32_16x16x32_bf16 v[26:29], v[86:89], v[90:93], v[26:29]
	ds_read_b128 v[86:89], v2 offset:10240
	s_waitcnt lgkmcnt(2)
	v_mfma_f32_16x16x32_bf16 v[54:57], v[74:77], v[82:85], v[54:57]
	v_mfma_f32_16x16x32_bf16 v[22:25], v[74:77], v[90:93], v[22:25]
	ds_read_b128 v[74:77], v2 offset:12288
	s_waitcnt lgkmcnt(2)
	v_mfma_f32_16x16x32_bf16 v[50:53], v[78:81], v[82:85], v[50:53]
	v_mfma_f32_16x16x32_bf16 v[18:21], v[78:81], v[90:93], v[18:21]
	ds_read_b128 v[78:81], v2 offset:14336
	v_add_u32_e32 v0, s2, v146
	s_waitcnt lgkmcnt(2)
	v_mfma_f32_16x16x32_bf16 v[46:49], v[86:89], v[82:85], v[46:49]
	v_mfma_f32_16x16x32_bf16 v[14:17], v[86:89], v[90:93], v[14:17]
	ds_read_b128 v[86:89], v0
	s_waitcnt lgkmcnt(2)
	v_mfma_f32_16x16x32_bf16 v[42:45], v[74:77], v[82:85], v[42:45]
	v_mfma_f32_16x16x32_bf16 v[10:13], v[74:77], v[90:93], v[10:13]
	ds_read_b128 v[74:77], v0 offset:2048
	s_waitcnt lgkmcnt(2)
	v_mfma_f32_16x16x32_bf16 v[38:41], v[78:81], v[82:85], v[38:41]
	v_cvt_pk_bf16_f32 v82, v202, v203
	v_cvt_pk_bf16_f32 v83, v204, v205
	v_cvt_pk_bf16_f32 v84, v206, v207
	v_mfma_f32_16x16x32_bf16 v[6:9], v[78:81], v[90:93], v[6:9]
	ds_read_b128 v[90:93], v0 offset:4096
	v_cvt_pk_bf16_f32 v78, v95, v96
	v_cvt_pk_bf16_f32 v79, v97, v98
	v_cvt_pk_bf16_f32 v80, v99, v100
	v_cvt_pk_bf16_f32 v81, v101, v135
	v_cvt_pk_bf16_f32 v85, v137, v208
	s_nop 0
	s_waitcnt lgkmcnt(2)
	v_mfma_f32_16x16x32_bf16 v[66:69], v[86:89], v[78:81], v[66:69]
	v_mfma_f32_16x16x32_bf16 v[34:37], v[86:89], v[82:85], v[34:37]
	ds_read_b128 v[86:89], v0 offset:6144
	s_waitcnt lgkmcnt(2)
	v_mfma_f32_16x16x32_bf16 v[62:65], v[74:77], v[78:81], v[62:65]
	v_mfma_f32_16x16x32_bf16 v[30:33], v[74:77], v[82:85], v[30:33]
	ds_read_b128 v[74:77], v0 offset:8192
	s_waitcnt lgkmcnt(2)
	v_mfma_f32_16x16x32_bf16 v[58:61], v[90:93], v[78:81], v[58:61]
	v_mfma_f32_16x16x32_bf16 v[26:29], v[90:93], v[82:85], v[26:29]
	ds_read_b128 v[90:93], v0 offset:10240
	s_waitcnt lgkmcnt(2)
	v_mfma_f32_16x16x32_bf16 v[54:57], v[86:89], v[78:81], v[54:57]
	v_mfma_f32_16x16x32_bf16 v[22:25], v[86:89], v[82:85], v[22:25]
	ds_read_b128 v[86:89], v0 offset:12288
	s_waitcnt lgkmcnt(2)
	v_mfma_f32_16x16x32_bf16 v[50:53], v[74:77], v[78:81], v[50:53]
	v_mfma_f32_16x16x32_bf16 v[18:21], v[74:77], v[82:85], v[18:21]
	ds_read_b128 v[74:77], v0 offset:14336
	s_waitcnt lgkmcnt(2)
	v_mfma_f32_16x16x32_bf16 v[46:49], v[90:93], v[78:81], v[46:49]
	v_mfma_f32_16x16x32_bf16 v[14:17], v[90:93], v[82:85], v[14:17]
	s_waitcnt lgkmcnt(1)
	v_mfma_f32_16x16x32_bf16 v[42:45], v[86:89], v[78:81], v[42:45]
	v_mfma_f32_16x16x32_bf16 v[10:13], v[86:89], v[82:85], v[10:13]
	s_waitcnt lgkmcnt(0)
	v_mfma_f32_16x16x32_bf16 v[38:41], v[74:77], v[78:81], v[38:41]
	s_waitcnt vmcnt(0)
	s_andn2_b64 vcc, exec, s[0:1]
	s_waitcnt vmcnt(0)
	v_mfma_f32_16x16x32_bf16 v[6:9], v[74:77], v[82:85], v[6:9]
	s_barrier
	s_cbranch_vccnz .LBB0_809
	s_branch .LBB0_518

.LBB0_902:
	s_or_b64 exec, exec, s[0:1]
	v_and_b32_e32 v0, 15, v38
	v_bitop3_b32 v40, v1, v0, 3 bitop3:0x6c
	v_bitop3_b32 v47, v1, v38, 3 bitop3:0x6c
	v_and_b32_e32 v51, 0x7f, v38
	v_lshlrev_b32_e32 v46, 4, v40
	v_lshlrev_b32_e32 v40, 7, v0
	v_lshlrev_b32_e32 v41, 3, v47
	s_movk_i32 s1, 0x70
	v_lshlrev_b32_e32 v142, 2, v51
	v_and_or_b32 v48, v41, s1, v40
	v_lshlrev_b32_e32 v40, 3, v1
	v_lshl_or_b32 v82, s6, 9, v142
	v_and_b32_e32 v49, 8, v40
	v_lshl_add_u64 v[40:41], s[74:75], 0, v[82:83]
	s_movk_i32 s6, 0x7000
	v_add_co_u32_e32 v42, vcc, s6, v40
	s_movk_i32 s6, 0x6000
	s_nop 0
	v_addc_co_u32_e32 v43, vcc, 0, v41, vcc
	global_load_dword v197, v82, s[76:77]
	global_load_dword v193, v[42:43], off offset:2048
	global_load_dword v194, v[42:43], off
	v_add_co_u32_e32 v42, vcc, s6, v40
	s_movk_i32 s6, 0x5000
	s_nop 0
	v_addc_co_u32_e32 v43, vcc, 0, v41, vcc
	global_load_dword v195, v[42:43], off offset:2048
	global_load_dword v196, v[42:43], off
	v_add_co_u32_e32 v42, vcc, s6, v40
	s_movk_i32 s6, 0x4000
	s_nop 0
	v_addc_co_u32_e32 v43, vcc, 0, v41, vcc
	global_load_dword v198, v[42:43], off offset:2048
	global_load_dword v199, v[42:43], off
	v_add_co_u32_e32 v42, vcc, s6, v40
	s_movk_i32 s43, 0x3000
	s_nop 0
	v_addc_co_u32_e32 v43, vcc, 0, v41, vcc
	global_load_dword v200, v[42:43], off offset:2048
	global_load_dword v201, v[42:43], off
	v_add_co_u32_e32 v42, vcc, s43, v40
	s_movk_i32 s6, 0x2000
	s_nop 0
	v_addc_co_u32_e32 v43, vcc, 0, v41, vcc
	global_load_dword v202, v[42:43], off offset:2048
	global_load_dword v203, v[42:43], off
	v_add_co_u32_e32 v42, vcc, s6, v40
	s_movk_i32 s6, 0x1000
	s_nop 0
	v_addc_co_u32_e32 v43, vcc, 0, v41, vcc
	v_add_co_u32_e32 v40, vcc, s6, v40
	global_load_dword v204, v[42:43], off offset:2048
	global_load_dword v205, v[42:43], off
	v_addc_co_u32_e32 v41, vcc, 0, v41, vcc
	global_load_dword v206, v[40:41], off offset:2048
	global_load_dword v207, v[40:41], off
	global_load_dword v209, v82, s[74:75] offset:2048
	global_load_dword v208, v82, s[74:75]
	s_ashr_i32 s0, s2, 6
	s_and_b32 s37, s0, 3
	s_ashr_i32 s3, s2, 8
	v_readlane_b32 s70, v252, 2
	v_readlane_b32 s71, v252, 3
	s_add_u32 s38, s70, 0x42490a00
	v_and_b32_e32 v44, 3, v1
	s_addc_u32 s39, s71, 0
	s_add_i32 s16, 0, 0x21800
	v_and_b32_e32 v42, 0xffffff00, v39
	v_and_b32_e32 v52, 0xfffffe00, v39
	v_lshlrev_b32_e32 v39, 5, v38
	s_and_b32 s2, s2, 0xffffff00
	s_add_i32 s6, 0, 0x20000
	v_and_b32_e32 v53, 0xffffffc0, v39
	v_and_b32_e32 v54, 32, v39
	v_lshl_or_b32 v147, v44, 3, s2
	s_add_i32 s2, s16, s2
	s_lshl_b32 s18, s37, 6
	v_lshlrev_b32_e32 v40, 2, v0
	v_add3_u32 v143, s6, v53, v54
	v_lshlrev_b32_e32 v51, 1, v51
	v_lshlrev_b32_e32 v54, 1, v38
	s_add_i32 s2, s2, s18
	s_add_i32 s18, s18, s16
	v_and_b32_e32 v54, 14, v54
	v_add_u32_e32 v148, s2, v40
	v_add_u32_e32 v149, s18, v40
	v_and_b32_e32 v40, 0xfffff000, v39
	v_and_b32_e32 v39, 0xf0, v51
	v_or3_b32 v151, v39, v54, v40
	v_mov_b32_e32 v39, 0x100
	v_bitop3_b32 v152, v151, 16, v39 bitop3:0x36
	v_mov_b32_e32 v39, 0x200
	v_bitop3_b32 v153, v151, 32, v39 bitop3:0x36
	v_mov_b32_e32 v39, 0x300
	v_bitop3_b32 v154, v151, 48, v39 bitop3:0x36
	v_mov_b32_e32 v39, 0x400
	v_bitop3_b32 v155, v151, 64, v39 bitop3:0x36
	s_movk_i32 s2, 0x50
	v_mov_b32_e32 v39, 0x500
	v_bitop3_b32 v156, v151, s2, v39 bitop3:0x36
	s_movk_i32 s66, 0x60
	v_mov_b32_e32 v39, 0x600
	v_bitop3_b32 v157, v151, s66, v39 bitop3:0x36
	v_mov_b32_e32 v39, 0x700
	v_bitop3_b32 v158, v151, s1, v39 bitop3:0x36
	s_movk_i32 s1, 0x80
	v_mov_b32_e32 v39, 0x800
	v_bitop3_b32 v159, v151, s1, v39 bitop3:0x36
	s_movk_i32 s2, 0x90
	v_mov_b32_e32 v39, 0x900
	v_ashrrev_i32_e32 v56, 8, v38
	v_bitop3_b32 v160, v151, s2, v39 bitop3:0x36
	s_movk_i32 s2, 0xa0
	v_mov_b32_e32 v39, 0xa00
	s_mov_b64 s[82:83], s[78:79]
	v_lshl_add_u32 v57, v56, 14, 0
	v_bfe_u32 v59, v38, 1, 3
	v_lshlrev_b32_e32 v56, 2, v56
	s_lshl_b32 s14, s37, 12
	v_bitop3_b32 v161, v151, s2, v39 bitop3:0x36
	s_movk_i32 s2, 0xb0
	v_mov_b32_e32 v39, 0xb00
	s_mov_b64 s[80:81], s[76:77]
	v_bitop3_b32 v60, v56, v140, 7 bitop3:0x78
	v_bitop3_b32 v61, v56, v59, 1 bitop3:0x36
	v_bitop3_b32 v62, v56, v59, 2 bitop3:0x36
	v_bitop3_b32 v56, v56, v59, 3 bitop3:0x36
	s_add_i32 s76, s14, 0
	v_lshlrev_b32_e32 v59, 2, v44
	s_lshl_b32 s14, s3, 15
	v_bitop3_b32 v162, v151, s2, v39 bitop3:0x36
	s_movk_i32 s2, 0xc0
	v_mov_b32_e32 v39, 0xc00
	v_ashrrev_i32_e32 v53, 7, v38
	s_lshl_b32 s17, s0, 3
	s_add_i32 s77, s14, 0
	s_lshl_b32 s14, s3, 14
	v_lshl_or_b32 v150, s3, 7, v59
	v_bitop3_b32 v163, v151, s2, v39 bitop3:0x36
	s_movk_i32 s3, 0xd0
	v_mov_b32_e32 v39, 0xd00
	v_lshl_add_u32 v144, v53, 10, s6
	s_add_i32 s6, 0, 0x21000
	v_bitop3_b32 v164, v151, s3, v39 bitop3:0x36
	s_movk_i32 s3, 0xe0
	v_mov_b32_e32 v39, 0xe00
	s_lshl_b32 s78, s0, 13
	s_or_b32 s0, s17, 1
	v_lshl_add_u32 v145, v38, 2, s6
	v_add_u32_e32 v146, s6, v142
	v_cmp_lt_i32_e64 s[6:7], 0, v53
	s_movk_i32 s44, 0xf0
	v_bitop3_b32 v165, v151, s3, v39 bitop3:0x36
	v_mov_b32_e32 v39, 0xf00
	s_lshl_b32 s3, s0, 2
	s_lshl_b32 s86, s0, 10
	s_or_b32 s0, s17, 2
	v_writelane_b32 v253, s6, 4
	v_bitop3_b32 v166, v151, s44, v39 bitop3:0x36
	v_lshlrev_b32_e32 v39, 4, v47
	v_bitop3_b32 v47, v44, v38, s3 bitop3:0x36
	s_lshl_b32 s3, s0, 2
	s_lshl_b32 s87, s0, 10
	s_or_b32 s0, s17, 5
	v_writelane_b32 v253, s7, 5
	v_cmp_lt_i32_e64 s[6:7], 1, v53
	v_cmp_lt_i32_e64 s[8:9], 2, v53
	v_cmp_lt_i32_e64 s[74:75], 3, v53
	v_add_u32_e32 v53, 0, v51
	v_bitop3_b32 v51, v44, v38, s3 bitop3:0x36
	s_lshl_b32 s3, s0, 2
	s_lshl_b32 s90, s0, 10
	s_or_b32 s0, s17, 6
	v_bitop3_b32 v54, v44, v38, s3 bitop3:0x36
	s_lshl_b32 s3, s0, 2
	v_and_b32_e32 v55, 0xff, v38
	s_add_i32 s72, 0, 0x18000
	v_bitop3_b32 v63, v44, v38, s3 bitop3:0x36
	v_bitop3_b32 v38, v44, v38, 12 bitop3:0x36
	v_lshlrev_b32_e32 v45, 8, v0
	v_lshlrev_b32_e32 v58, 1, v55
	v_lshl_add_u32 v55, v55, 7, s72
	s_add_i32 s76, s76, 0x14000
	s_add_i32 s72, s72, s14
	s_or_b32 s88, s78, 0xc00
	s_or_b32 s89, s78, 0x1000
	s_lshl_b32 s91, s0, 10
	v_lshlrev_b32_e32 v64, 4, v38
	s_or_b32 s92, s78, 0x1c00
	v_or_b32_e32 v38, 2, v59
	v_bitop3_b32 v169, v46, s2, v45 bitop3:0x36
	s_cmp_eq_u32 s37, 0
	v_cmp_gt_u32_e64 s[2:3], v38, v0
	v_or_b32_e32 v38, 3, v59
	v_bitop3_b32 v168, v46, s1, v45 bitop3:0x36
	s_cselect_b64 s[62:63], -1, 0
	v_cmp_gt_u32_e32 vcc, v59, v0
	v_cmp_ge_u32_e64 s[0:1], v59, v0
	v_cmp_gt_u32_e64 s[22:23], v38, v0
	s_and_b64 s[56:57], s[62:63], vcc
	s_and_b64 s[40:41], s[62:63], s[0:1]
	s_and_b64 s[48:49], s[62:63], s[2:3]
	s_and_b64 s[50:51], s[62:63], s[22:23]
	s_cmp_eq_u32 s37, 1
	s_cselect_b64 s[18:19], -1, 0
	s_and_b64 s[20:21], s[18:19], vcc
	s_and_b64 s[46:47], s[18:19], s[0:1]
	s_and_b64 s[60:61], s[18:19], s[2:3]
	s_and_b64 s[64:65], s[18:19], s[22:23]
	s_cmp_gt_u32 s37, 1
	s_cselect_b64 s[52:53], -1, 0
	s_cmp_eq_u32 s37, 2
	v_writelane_b32 v253, s8, 6
	s_cselect_b64 s[58:59], -1, 0
	v_lshlrev_b32_e32 v82, 2, v150
	v_writelane_b32 v253, s9, 7
	s_and_b64 s[8:9], s[58:59], vcc
	v_writelane_b32 v253, s8, 8
	v_or_b32_e32 v170, 16, v150
	v_lshl_add_u64 v[84:85], s[82:83], 0, v[82:83]
	v_writelane_b32 v253, s9, 9
	s_and_b64 s[8:9], s[58:59], s[0:1]
	v_writelane_b32 v253, s8, 10
	v_lshlrev_b32_e32 v82, 2, v170
	v_or_b32_e32 v171, 32, v150
	v_writelane_b32 v253, s9, 11
	s_and_b64 s[8:9], s[58:59], s[2:3]
	v_lshl_add_u64 v[86:87], s[82:83], 0, v[82:83]
	v_lshlrev_b32_e32 v82, 2, v171
	v_or_b32_e32 v172, 48, v150
	v_writelane_b32 v253, s8, 12
	v_lshl_add_u64 v[88:89], s[82:83], 0, v[82:83]
	v_lshlrev_b32_e32 v82, 2, v172
	v_or_b32_e32 v173, 64, v150
	v_writelane_b32 v253, s9, 13
	s_and_b64 s[8:9], s[58:59], s[22:23]
	v_lshl_add_u64 v[90:91], s[82:83], 0, v[82:83]
	v_lshlrev_b32_e32 v82, 2, v173
	v_or_b32_e32 v174, 0x50, v150
	s_cmp_lg_u32 s37, 3
	v_lshl_add_u64 v[92:93], s[82:83], 0, v[82:83]
	v_lshlrev_b32_e32 v82, 2, v174
	v_or_b32_e32 v175, 0x60, v150
	v_writelane_b32 v253, s8, 14
	s_cselect_b64 s[68:69], -1, 0
	v_lshl_add_u64 v[94:95], s[82:83], 0, v[82:83]
	v_lshlrev_b32_e32 v82, 2, v175
	v_or_b32_e32 v176, 0x70, v150
	v_or_b32_e32 v141, v46, v45
	v_or_b32_e32 v50, v48, v49
	v_bitop3_b32 v167, v46, 64, v45 bitop3:0x36
	v_writelane_b32 v253, s9, 15
	v_bitop3_b32 v45, v48, 32, v49 bitop3:0x36
	v_bitop3_b32 v46, v48, 64, v49 bitop3:0x36
	v_bitop3_b32 v48, v48, s66, v49 bitop3:0x36
	v_lshl_add_u64 v[96:97], s[82:83], 0, v[82:83]
	v_lshlrev_b32_e32 v82, 2, v176
	s_or_b64 s[58:59], s[62:63], s[20:21]
	s_or_b64 s[46:47], s[62:63], s[46:47]
	s_or_b64 s[60:61], s[62:63], s[60:61]
	s_or_b64 s[62:63], s[62:63], s[64:65]
	s_or_b64 s[8:9], s[68:69], s[22:23]
	s_or_b64 s[2:3], s[68:69], s[2:3]
	s_or_b64 s[66:67], s[68:69], s[0:1]
	s_or_b64 s[64:65], s[68:69], vcc
	v_lshl_or_b32 v177, s37, 4, v0
	v_lshl_or_b32 v0, v44, 8, s78
	v_readlane_b32 s68, v252, 0
	v_lshlrev_b32_e32 v47, 4, v47
	v_lshlrev_b32_e32 v54, 4, v54
	v_lshl_add_u64 v[98:99], s[82:83], 0, v[82:83]
	v_and_or_b32 v82, v39, s44, v0
	s_mov_b64 s[0:1], 0x50890a00
	v_readlane_b32 s69, v252, 1
	s_mov_b32 s96, s68
	s_ashr_i32 s97, s68, 31
	s_movk_i32 s45, 0x400
	v_and_b32_e32 v47, 0xf0, v47
	v_lshlrev_b32_e32 v51, 4, v51
	v_and_b32_e32 v54, 0xf0, v54
	v_lshlrev_b32_e32 v63, 4, v63
	v_lshl_add_u64 v[100:101], v[82:83], 0, s[0:1]
	s_lshl_b64 s[68:69], s[96:97], 16
	v_or_b32_e32 v82, 0x1000, v82
	s_movk_i32 s37, 0x1400
	s_movk_i32 s73, 0x800
	v_and_b32_e32 v51, 0xf0, v51
	v_and_b32_e32 v63, 0xf0, v63
	s_add_u32 s68, s70, s68
	v_or3_b32 v38, v0, v47, s45
	v_mov_b32_e32 v39, v83
	v_lshl_add_u64 v[108:109], v[82:83], 0, s[0:1]
	v_or3_b32 v82, v0, v54, s37
	s_movk_i32 s37, 0x1800
	v_cmp_eq_u32_e64 s[54:55], 0, v44
	s_addc_u32 s69, s71, s69
	v_readlane_b32 s70, v252, 6
	v_lshl_add_u64 v[102:103], v[38:39], 0, s[0:1]
	v_or3_b32 v38, v0, v51, s73
	v_and_or_b32 v44, v64, s44, v0
	v_lshl_add_u64 v[110:111], v[82:83], 0, s[0:1]
	v_or3_b32 v82, v0, v63, s37
	s_mov_b32 s80, s70
	v_lshl_add_u64 v[104:105], v[38:39], 0, s[0:1]
	v_or_b32_e32 v38, 0xc00, v44
	v_lshl_add_u64 v[112:113], v[82:83], 0, s[0:1]
	v_or_b32_e32 v82, 0x1c00, v44
	v_lshl_add_u64 v[106:107], v[38:39], 0, s[0:1]
	v_lshl_add_u64 v[114:115], v[82:83], 0, s[0:1]
	s_mov_b32 s0, s80
	v_readlane_b32 s71, v252, 7
	v_writelane_b32 v252, s0, 6
	v_add_u32_e32 v41, 0, v132
	v_add_u32_e32 v43, 0, v134
	v_writelane_b32 v252, s1, 7
	s_mov_b32 s0, s96
	v_lshlrev_b32_e32 v60, 4, v60
	v_lshlrev_b32_e32 v61, 4, v61
	v_lshlrev_b32_e32 v62, 4, v62
	v_lshlrev_b32_e32 v56, 4, v56
	v_writelane_b32 v253, s8, 16
	s_ashr_i32 s81, s70, 31
	v_writelane_b32 v252, s0, 0
	s_mov_b32 s42, 0
	v_writelane_b32 v253, s9, 17
	s_lshl_b64 s[70:71], s[80:81], 16
	s_lshl_b32 s79, s80, 6
	s_lshl_b32 s80, s80, 4
	v_add_u32_e32 v178, v41, v42
	v_add_u32_e32 v179, v43, v52
	s_mov_b32 s81, 0xbfb8aa3b
	s_mov_b32 s82, 0x800000
	s_mov_b32 s83, 0x3f317217
	s_mov_b32 s84, 0x7f800000
	v_add_u32_e32 v180, v53, v40
	s_add_i32 s85, 0, 0x10000
	v_add_u32_e32 v181, v57, v58
	v_add_u32_e32 v182, v55, v60
	v_add_u32_e32 v183, v55, v61
	v_add_u32_e32 v184, v55, v62
	v_add_u32_e32 v185, v55, v56
	s_add_i32 s86, s86, 0
	s_add_i32 s87, s87, 0
	s_add_i32 s88, s88, 0
	s_add_i32 s89, s89, 0
	s_add_i32 s90, s90, 0
	s_add_i32 s91, s91, 0
	s_add_i32 s92, s92, 0
	s_add_i32 s93, 0, 0x11000
	s_add_i32 s94, 0, 0x12000
	s_add_i32 s95, 0, 0x13000
	v_add_u32_e32 v186, s72, v50
	v_add_u32_e32 v187, s72, v45
	v_add_u32_e32 v188, s72, v46
	v_add_u32_e32 v189, s72, v48
	v_mov_b32_e32 v190, 0x3727c5ac
	v_mov_b32_e32 v191, 0x260
	v_mov_b32_e32 v192, 0x41b17218
	v_writelane_b32 v252, s1, 1
	s_branch .LBB0_904
	s_nop 0
	s_nop 0
	s_nop 0
	s_nop 0
